# K-loop compute-segment head: redundant post-barrier lgkmcnt(0) deleted and s_setprio 1 moved before the barrier, so the first MFMA follows the barrier release directly (on top of peel+nt+norm1 de-seri
# speedup vs baseline: 1.0071x; 1.0071x over previous
.LBB0_310:
	s_ashr_i32 s91, s90, 31
	s_lshl_b64 s[4:5], s[90:91], 20
	s_add_u32 s62, s66, s4
	s_addc_u32 s63, s67, s5
	s_and_b64 s[4:5], s[36:37], exec
	s_cselect_b32 s4, s63, s25
	s_cselect_b32 s5, s62, s24
	s_ashr_i32 s89, s88, 31
	s_lshl_b64 s[20:21], s[88:89], 20
	s_add_u32 s20, s72, s20
	s_addc_u32 s21, s73, s21
	s_and_b64 s[30:31], s[36:37], exec
	s_cselect_b32 s8, s21, s1
	s_cselect_b32 s13, s20, s0
	s_add_u32 s17, s0, 0x10000
	s_addc_u32 s19, s1, 0
	s_add_u32 s0, s24, 0x80080
	s_addc_u32 s1, s25, 0
	s_mov_b32 s28, -2
	v_add_u32_e32 v100, s3, v190
	v_add_u32_e32 v156, s75, v190
	ds_read_b128 v[40:43], v100
	ds_read_b128 v[60:63], v100 offset:1024
	ds_read_b128 v[80:83], v100 offset:2048
	ds_read_b128 v[100:103], v100 offset:3072
	ds_read_b128 v[120:123], v156
	ds_read_b128 v[140:143], v156 offset:1024
	ds_read_b128 v[152:155], v156 offset:2048
	ds_read_b128 v[156:159], v156 offset:3072
	s_add_u32 s24, s0, 0xfff80080
	s_addc_u32 s25, s1, -1
	s_cmp_eq_u32 s28, 28
	s_cselect_b32 s39, s4, s25
	s_cselect_b32 s38, s5, s24
	s_cselect_b32 s25, s8, s19
	s_cselect_b32 s24, s13, s17
	v_lshl_add_u64 v[188:189], s[0:1], 0, v[168:169]
	s_add_i32 m0, s78, 0xc000
	ds_read_b128 v[172:175], v191
	ds_read_b128 v[176:179], v191 offset:1024
	ds_read_b128 v[180:183], v191 offset:2048
	ds_read_b128 v[184:187], v191 offset:3072
	ds_read_b128 v[192:195], v191 offset:4096
	ds_read_b128 v[196:199], v191 offset:5120
	ds_read_b128 v[200:203], v191 offset:6144
	ds_read_b128 v[204:207], v191 offset:7168
	global_load_lds_dwordx4 v[188:189], off
	v_lshl_add_u64 v[188:189], s[0:1], 0, v[170:171]
	s_add_i32 m0, s78, 0xe000
	s_nop 0
	global_load_lds_dwordx4 v[188:189], off
	s_waitcnt vmcnt(8)
	s_waitcnt lgkmcnt(0)
	s_setprio 1
	s_barrier
	v_mfma_f32_16x16x32_bf16 v[148:151], v[40:43], v[172:175], 0
	v_mfma_f32_16x16x32_bf16 v[144:147], v[80:83], v[172:175], 0
	v_mfma_f32_16x16x32_bf16 v[128:131], v[40:43], v[180:183], 0
	v_mfma_f32_16x16x32_bf16 v[124:127], v[80:83], v[180:183], 0
	v_mfma_f32_16x16x32_bf16 v[108:111], v[40:43], v[192:195], 0
	v_mfma_f32_16x16x32_bf16 v[104:107], v[80:83], v[192:195], 0
	v_mfma_f32_16x16x32_bf16 v[88:91], v[40:43], v[200:203], 0
	v_mfma_f32_16x16x32_bf16 v[84:87], v[80:83], v[200:203], 0
	v_mfma_f32_16x16x32_bf16 v[148:151], v[60:63], v[176:179], v[148:151]
	v_mfma_f32_16x16x32_bf16 v[144:147], v[100:103], v[176:179], v[144:147]
	v_mfma_f32_16x16x32_bf16 v[128:131], v[60:63], v[184:187], v[128:131]
	v_mfma_f32_16x16x32_bf16 v[124:127], v[100:103], v[184:187], v[124:127]
	v_mfma_f32_16x16x32_bf16 v[108:111], v[60:63], v[196:199], v[108:111]
	v_mfma_f32_16x16x32_bf16 v[104:107], v[100:103], v[196:199], v[104:107]
	v_mfma_f32_16x16x32_bf16 v[88:91], v[60:63], v[204:207], v[88:91]
	v_mfma_f32_16x16x32_bf16 v[84:87], v[100:103], v[204:207], v[84:87]
	s_setprio 0
	s_setprio 1
	v_mfma_f32_16x16x32_bf16 v[136:139], v[120:123], v[172:175], 0
	v_mfma_f32_16x16x32_bf16 v[132:135], v[152:155], v[172:175], 0
	v_mfma_f32_16x16x32_bf16 v[116:119], v[120:123], v[180:183], 0
	v_mfma_f32_16x16x32_bf16 v[112:115], v[152:155], v[180:183], 0
	v_mfma_f32_16x16x32_bf16 v[96:99], v[120:123], v[192:195], 0
	v_mfma_f32_16x16x32_bf16 v[92:95], v[152:155], v[192:195], 0
	v_mfma_f32_16x16x32_bf16 v[76:79], v[120:123], v[200:203], 0
	v_mfma_f32_16x16x32_bf16 v[72:75], v[152:155], v[200:203], 0
	v_mfma_f32_16x16x32_bf16 v[136:139], v[140:143], v[176:179], v[136:139]
	v_mfma_f32_16x16x32_bf16 v[132:135], v[156:159], v[176:179], v[132:135]
	v_mfma_f32_16x16x32_bf16 v[116:119], v[140:143], v[184:187], v[116:119]
	v_mfma_f32_16x16x32_bf16 v[112:115], v[156:159], v[184:187], v[112:115]
	v_mfma_f32_16x16x32_bf16 v[96:99], v[140:143], v[196:199], v[96:99]
	v_mfma_f32_16x16x32_bf16 v[92:95], v[156:159], v[196:199], v[92:95]
	v_mfma_f32_16x16x32_bf16 v[76:79], v[140:143], v[204:207], v[76:79]
	v_mfma_f32_16x16x32_bf16 v[72:75], v[156:159], v[204:207], v[72:75]
	s_setprio 0
	s_barrier
	s_mov_b32 m0, s23
	v_lshl_add_u64 v[188:189], s[24:25], 0, v[162:163]
	s_add_u32 s30, s24, 0x4000
	ds_read_b128 v[172:175], v191 offset:16384
	ds_read_b128 v[176:179], v191 offset:17408
	ds_read_b128 v[180:183], v191 offset:18432
	ds_read_b128 v[184:187], v191 offset:19456
	ds_read_b128 v[192:195], v191 offset:20480
	ds_read_b128 v[196:199], v191 offset:21504
	ds_read_b128 v[200:203], v191 offset:22528
	ds_read_b128 v[204:207], v191 offset:23552
	global_load_lds_dwordx4 v[188:189], off
	v_lshl_add_u64 v[188:189], s[24:25], 0, v[166:167]
	s_mov_b32 m0, s74
	s_addc_u32 s31, s25, 0
	global_load_lds_dwordx4 v[188:189], off
	v_lshl_add_u64 v[188:189], s[30:31], 0, v[162:163]
	s_mov_b32 m0, s76
	v_lshl_add_u64 v[208:209], s[38:39], 0, v[164:165]
	global_load_lds_dwordx4 v[188:189], off
	v_lshl_add_u64 v[188:189], s[30:31], 0, v[166:167]
	s_mov_b32 m0, s77
	s_nop 0
	global_load_lds_dwordx4 v[188:189], off
	v_lshl_add_u64 v[188:189], s[38:39], 0, v[160:161]
	s_mov_b32 m0, s78
	s_nop 0
	global_load_lds_dwordx4 v[188:189], off
	s_mov_b32 m0, s79
	s_nop 0
	global_load_lds_dwordx4 v[208:209], off
	s_waitcnt vmcnt(8)
	s_waitcnt lgkmcnt(0)
	s_setprio 1
	s_barrier
	v_mfma_f32_16x16x32_bf16 v[68:71], v[40:43], v[172:175], 0
	v_mfma_f32_16x16x32_bf16 v[64:67], v[80:83], v[172:175], 0
	v_mfma_f32_16x16x32_bf16 v[48:51], v[40:43], v[180:183], 0
	v_mfma_f32_16x16x32_bf16 v[44:47], v[80:83], v[180:183], 0
	v_mfma_f32_16x16x32_bf16 v[28:31], v[40:43], v[192:195], 0
	v_mfma_f32_16x16x32_bf16 v[24:27], v[80:83], v[192:195], 0
	v_mfma_f32_16x16x32_bf16 v[12:15], v[40:43], v[200:203], 0
	v_mfma_f32_16x16x32_bf16 v[8:11], v[80:83], v[200:203], 0
	v_mfma_f32_16x16x32_bf16 v[68:71], v[60:63], v[176:179], v[68:71]
	v_mfma_f32_16x16x32_bf16 v[64:67], v[100:103], v[176:179], v[64:67]
	v_mfma_f32_16x16x32_bf16 v[48:51], v[60:63], v[184:187], v[48:51]
	v_mfma_f32_16x16x32_bf16 v[44:47], v[100:103], v[184:187], v[44:47]
	v_mfma_f32_16x16x32_bf16 v[28:31], v[60:63], v[196:199], v[28:31]
	v_mfma_f32_16x16x32_bf16 v[24:27], v[100:103], v[196:199], v[24:27]
	v_mfma_f32_16x16x32_bf16 v[12:15], v[60:63], v[204:207], v[12:15]
	v_mfma_f32_16x16x32_bf16 v[8:11], v[100:103], v[204:207], v[8:11]
	s_setprio 0
	s_setprio 1
	v_mfma_f32_16x16x32_bf16 v[52:55], v[152:155], v[172:175], 0
	v_mfma_f32_16x16x32_bf16 v[36:39], v[120:123], v[180:183], 0
	v_mfma_f32_16x16x32_bf16 v[32:35], v[152:155], v[180:183], 0
	v_mfma_f32_16x16x32_bf16 v[20:23], v[120:123], v[192:195], 0
	v_mfma_f32_16x16x32_bf16 v[16:19], v[152:155], v[192:195], 0
	v_mfma_f32_16x16x32_bf16 v[4:7], v[120:123], v[200:203], 0
	v_mfma_f32_16x16x32_bf16 v[0:3], v[152:155], v[200:203], 0
	v_mfma_f32_16x16x32_bf16 v[40:43], v[120:123], v[172:175], 0
	v_mfma_f32_16x16x32_bf16 v[52:55], v[156:159], v[176:179], v[52:55]
	v_mfma_f32_16x16x32_bf16 v[36:39], v[140:143], v[184:187], v[36:39]
	v_mfma_f32_16x16x32_bf16 v[32:35], v[156:159], v[184:187], v[32:35]
	v_mfma_f32_16x16x32_bf16 v[20:23], v[140:143], v[196:199], v[20:23]
	v_mfma_f32_16x16x32_bf16 v[16:19], v[156:159], v[196:199], v[16:19]
	v_mfma_f32_16x16x32_bf16 v[4:7], v[140:143], v[204:207], v[4:7]
	v_mfma_f32_16x16x32_bf16 v[0:3], v[156:159], v[204:207], v[0:3]
	v_mfma_f32_16x16x32_bf16 v[40:43], v[140:143], v[176:179], v[40:43]
	s_setprio 0
	s_barrier
	v_add_u32_e32 v100, s86, v190
	v_add_u32_e32 v156, s95, v190
	ds_read_b128 v[56:59], v100
	ds_read_b128 v[60:63], v100 offset:1024
	ds_read_b128 v[80:83], v100 offset:2048
	ds_read_b128 v[100:103], v100 offset:3072
	ds_read_b128 v[120:123], v156
	ds_read_b128 v[140:143], v156 offset:1024
	ds_read_b128 v[152:155], v156 offset:2048
	ds_read_b128 v[156:159], v156 offset:3072
	s_add_u32 s30, s38, 0x80000
	s_addc_u32 s31, s39, 0
	s_mov_b32 m0, s82
	v_lshl_add_u64 v[210:211], s[30:31], 0, v[160:161]
	ds_read_b128 v[172:175], v191 offset:32768
	ds_read_b128 v[176:179], v191 offset:33792
	ds_read_b128 v[180:183], v191 offset:34816
	ds_read_b128 v[184:187], v191 offset:35840
	ds_read_b128 v[192:195], v191 offset:36864
	ds_read_b128 v[196:199], v191 offset:37888
	ds_read_b128 v[200:203], v191 offset:38912
	ds_read_b128 v[204:207], v191 offset:39936
	global_load_lds_dwordx4 v[210:211], off
	v_lshl_add_u64 v[210:211], s[30:31], 0, v[164:165]
	s_mov_b32 m0, s83
	s_nop 0
	global_load_lds_dwordx4 v[210:211], off
	s_waitcnt vmcnt(8)
	s_waitcnt lgkmcnt(0)
	s_setprio 1
	s_barrier
	v_mfma_f32_16x16x32_bf16 v[148:151], v[56:59], v[172:175], v[148:151]
	v_mfma_f32_16x16x32_bf16 v[144:147], v[80:83], v[172:175], v[144:147]
	v_mfma_f32_16x16x32_bf16 v[128:131], v[56:59], v[180:183], v[128:131]
	v_mfma_f32_16x16x32_bf16 v[124:127], v[80:83], v[180:183], v[124:127]
	v_mfma_f32_16x16x32_bf16 v[108:111], v[56:59], v[192:195], v[108:111]
	v_mfma_f32_16x16x32_bf16 v[104:107], v[80:83], v[192:195], v[104:107]
	v_mfma_f32_16x16x32_bf16 v[88:91], v[56:59], v[200:203], v[88:91]
	v_mfma_f32_16x16x32_bf16 v[84:87], v[80:83], v[200:203], v[84:87]
	v_mfma_f32_16x16x32_bf16 v[148:151], v[60:63], v[176:179], v[148:151]
	v_mfma_f32_16x16x32_bf16 v[144:147], v[100:103], v[176:179], v[144:147]
	v_mfma_f32_16x16x32_bf16 v[128:131], v[60:63], v[184:187], v[128:131]
	v_mfma_f32_16x16x32_bf16 v[124:127], v[100:103], v[184:187], v[124:127]
	v_mfma_f32_16x16x32_bf16 v[108:111], v[60:63], v[196:199], v[108:111]
	v_mfma_f32_16x16x32_bf16 v[104:107], v[100:103], v[196:199], v[104:107]
	v_mfma_f32_16x16x32_bf16 v[88:91], v[60:63], v[204:207], v[88:91]
	v_mfma_f32_16x16x32_bf16 v[84:87], v[100:103], v[204:207], v[84:87]
	s_setprio 0
	s_setprio 1
	v_mfma_f32_16x16x32_bf16 v[136:139], v[120:123], v[172:175], v[136:139]
	v_mfma_f32_16x16x32_bf16 v[132:135], v[152:155], v[172:175], v[132:135]
	v_mfma_f32_16x16x32_bf16 v[116:119], v[120:123], v[180:183], v[116:119]
	v_mfma_f32_16x16x32_bf16 v[112:115], v[152:155], v[180:183], v[112:115]
	v_mfma_f32_16x16x32_bf16 v[96:99], v[120:123], v[192:195], v[96:99]
	v_mfma_f32_16x16x32_bf16 v[92:95], v[152:155], v[192:195], v[92:95]
	v_mfma_f32_16x16x32_bf16 v[76:79], v[120:123], v[200:203], v[76:79]
	v_mfma_f32_16x16x32_bf16 v[72:75], v[152:155], v[200:203], v[72:75]
	v_mfma_f32_16x16x32_bf16 v[136:139], v[140:143], v[176:179], v[136:139]
	v_mfma_f32_16x16x32_bf16 v[132:135], v[156:159], v[176:179], v[132:135]
	v_mfma_f32_16x16x32_bf16 v[116:119], v[140:143], v[184:187], v[116:119]
	v_mfma_f32_16x16x32_bf16 v[112:115], v[156:159], v[184:187], v[112:115]
	v_mfma_f32_16x16x32_bf16 v[96:99], v[140:143], v[196:199], v[96:99]
	v_mfma_f32_16x16x32_bf16 v[92:95], v[156:159], v[196:199], v[92:95]
	v_mfma_f32_16x16x32_bf16 v[76:79], v[140:143], v[204:207], v[76:79]
	v_mfma_f32_16x16x32_bf16 v[72:75], v[156:159], v[204:207], v[72:75]
	s_setprio 0
	s_barrier
	s_add_u32 s30, s24, 0x8000
	s_addc_u32 s31, s25, 0
	s_mov_b32 m0, s87
	v_lshl_add_u64 v[210:211], s[30:31], 0, v[162:163]
	s_add_u32 s24, s24, 0xc000
	ds_read_b128 v[172:175], v191 offset:49152
	ds_read_b128 v[176:179], v191 offset:50176
	ds_read_b128 v[180:183], v191 offset:51200
	ds_read_b128 v[184:187], v191 offset:52224
	ds_read_b128 v[192:195], v191 offset:53248
	ds_read_b128 v[196:199], v191 offset:54272
	ds_read_b128 v[200:203], v191 offset:55296
	ds_read_b128 v[204:207], v191 offset:56320
	global_load_lds_dwordx4 v[210:211], off
	v_lshl_add_u64 v[210:211], s[30:31], 0, v[166:167]
	s_mov_b32 m0, s92
	s_addc_u32 s25, s25, 0
	global_load_lds_dwordx4 v[210:211], off
	v_lshl_add_u64 v[210:211], s[24:25], 0, v[162:163]
	s_mov_b32 m0, s96
	v_lshl_add_u64 v[188:189], v[188:189], 0, s[26:27]
	global_load_lds_dwordx4 v[210:211], off
	v_lshl_add_u64 v[210:211], s[24:25], 0, v[166:167]
	s_mov_b32 m0, s97
	s_nop 0
	global_load_lds_dwordx4 v[210:211], off
	s_mov_b32 m0, s93
	s_nop 0
	global_load_lds_dwordx4 v[188:189], off
	v_lshl_add_u64 v[188:189], v[208:209], 0, s[26:27]
	s_mov_b32 m0, s94
	s_nop 0
	global_load_lds_dwordx4 v[188:189], off
	s_waitcnt vmcnt(8)
	s_waitcnt lgkmcnt(0)
	s_setprio 1
	s_barrier
	v_mfma_f32_16x16x32_bf16 v[68:71], v[56:59], v[172:175], v[68:71]
	v_mfma_f32_16x16x32_bf16 v[64:67], v[80:83], v[172:175], v[64:67]
	v_mfma_f32_16x16x32_bf16 v[48:51], v[56:59], v[180:183], v[48:51]
	v_mfma_f32_16x16x32_bf16 v[44:47], v[80:83], v[180:183], v[44:47]
	v_mfma_f32_16x16x32_bf16 v[28:31], v[56:59], v[192:195], v[28:31]
	v_mfma_f32_16x16x32_bf16 v[24:27], v[80:83], v[192:195], v[24:27]
	v_mfma_f32_16x16x32_bf16 v[12:15], v[56:59], v[200:203], v[12:15]
	v_mfma_f32_16x16x32_bf16 v[8:11], v[80:83], v[200:203], v[8:11]
	v_mfma_f32_16x16x32_bf16 v[68:71], v[60:63], v[176:179], v[68:71]
	v_mfma_f32_16x16x32_bf16 v[64:67], v[100:103], v[176:179], v[64:67]
	v_mfma_f32_16x16x32_bf16 v[48:51], v[60:63], v[184:187], v[48:51]
	v_mfma_f32_16x16x32_bf16 v[44:47], v[100:103], v[184:187], v[44:47]
	v_mfma_f32_16x16x32_bf16 v[28:31], v[60:63], v[196:199], v[28:31]
	v_mfma_f32_16x16x32_bf16 v[24:27], v[100:103], v[196:199], v[24:27]
	v_mfma_f32_16x16x32_bf16 v[12:15], v[60:63], v[204:207], v[12:15]
	v_mfma_f32_16x16x32_bf16 v[8:11], v[100:103], v[204:207], v[8:11]
	s_setprio 0
	s_setprio 1
	v_mfma_f32_16x16x32_bf16 v[40:43], v[120:123], v[172:175], v[40:43]
	v_mfma_f32_16x16x32_bf16 v[56:59], v[140:143], v[176:179], v[40:43]
	v_mfma_f32_16x16x32_bf16 v[40:43], v[152:155], v[172:175], v[52:55]
	v_mfma_f32_16x16x32_bf16 v[36:39], v[120:123], v[180:183], v[36:39]
	v_mfma_f32_16x16x32_bf16 v[32:35], v[152:155], v[180:183], v[32:35]
	v_mfma_f32_16x16x32_bf16 v[20:23], v[120:123], v[192:195], v[20:23]
	v_mfma_f32_16x16x32_bf16 v[16:19], v[152:155], v[192:195], v[16:19]
	v_mfma_f32_16x16x32_bf16 v[4:7], v[120:123], v[200:203], v[4:7]
	v_mfma_f32_16x16x32_bf16 v[0:3], v[152:155], v[200:203], v[0:3]
	v_mfma_f32_16x16x32_bf16 v[52:55], v[156:159], v[176:179], v[40:43]
	v_mfma_f32_16x16x32_bf16 v[36:39], v[140:143], v[184:187], v[36:39]
	v_mfma_f32_16x16x32_bf16 v[32:35], v[156:159], v[184:187], v[32:35]
	v_mfma_f32_16x16x32_bf16 v[20:23], v[140:143], v[196:199], v[20:23]
	v_mfma_f32_16x16x32_bf16 v[16:19], v[156:159], v[196:199], v[16:19]
	v_mfma_f32_16x16x32_bf16 v[4:7], v[140:143], v[204:207], v[4:7]
	v_mfma_f32_16x16x32_bf16 v[0:3], v[156:159], v[204:207], v[0:3]
	s_setprio 0
	s_barrier
	s_add_i32 s28, s28, 2
	s_add_u32 s17, s17, 0x10000
	s_addc_u32 s19, s19, 0
	s_add_u32 s0, s0, 0x100
	s_addc_u32 s1, s1, 0
	s_cmp_gt_u32 s28, 29
.LBB0_311:
	v_add_u32_e32 v100, s3, v190
	v_add_u32_e32 v156, s75, v190
	ds_read_b128 v[40:43], v100
	ds_read_b128 v[60:63], v100 offset:1024
	ds_read_b128 v[80:83], v100 offset:2048
	ds_read_b128 v[100:103], v100 offset:3072
	ds_read_b128 v[120:123], v156
	ds_read_b128 v[140:143], v156 offset:1024
	ds_read_b128 v[152:155], v156 offset:2048
	ds_read_b128 v[156:159], v156 offset:3072
	s_add_u32 s24, s0, 0xfff80080
	s_addc_u32 s25, s1, -1
	s_cmp_eq_u32 s28, 28
	s_cselect_b32 s39, s4, s25
	s_cselect_b32 s38, s5, s24
	s_cselect_b32 s25, s8, s19
	s_cselect_b32 s24, s13, s17
	v_lshl_add_u64 v[188:189], s[0:1], 0, v[168:169]
	s_add_i32 m0, s78, 0xc000
	ds_read_b128 v[172:175], v191
	ds_read_b128 v[176:179], v191 offset:1024
	ds_read_b128 v[180:183], v191 offset:2048
	ds_read_b128 v[184:187], v191 offset:3072
	ds_read_b128 v[192:195], v191 offset:4096
	ds_read_b128 v[196:199], v191 offset:5120
	ds_read_b128 v[200:203], v191 offset:6144
	ds_read_b128 v[204:207], v191 offset:7168
	global_load_lds_dwordx4 v[188:189], off
	v_lshl_add_u64 v[188:189], s[0:1], 0, v[170:171]
	s_add_i32 m0, s78, 0xe000
	s_nop 0
	global_load_lds_dwordx4 v[188:189], off
	s_waitcnt vmcnt(8)
	s_waitcnt lgkmcnt(0)
	s_setprio 1
	s_barrier
	v_mfma_f32_16x16x32_bf16 v[148:151], v[40:43], v[172:175], v[148:151]
	v_mfma_f32_16x16x32_bf16 v[144:147], v[80:83], v[172:175], v[144:147]
	v_mfma_f32_16x16x32_bf16 v[128:131], v[40:43], v[180:183], v[128:131]
	v_mfma_f32_16x16x32_bf16 v[124:127], v[80:83], v[180:183], v[124:127]
	v_mfma_f32_16x16x32_bf16 v[108:111], v[40:43], v[192:195], v[108:111]
	v_mfma_f32_16x16x32_bf16 v[104:107], v[80:83], v[192:195], v[104:107]
	v_mfma_f32_16x16x32_bf16 v[88:91], v[40:43], v[200:203], v[88:91]
	v_mfma_f32_16x16x32_bf16 v[84:87], v[80:83], v[200:203], v[84:87]
	v_mfma_f32_16x16x32_bf16 v[148:151], v[60:63], v[176:179], v[148:151]
	v_mfma_f32_16x16x32_bf16 v[144:147], v[100:103], v[176:179], v[144:147]
	v_mfma_f32_16x16x32_bf16 v[128:131], v[60:63], v[184:187], v[128:131]
	v_mfma_f32_16x16x32_bf16 v[124:127], v[100:103], v[184:187], v[124:127]
	v_mfma_f32_16x16x32_bf16 v[108:111], v[60:63], v[196:199], v[108:111]
	v_mfma_f32_16x16x32_bf16 v[104:107], v[100:103], v[196:199], v[104:107]
	v_mfma_f32_16x16x32_bf16 v[88:91], v[60:63], v[204:207], v[88:91]
	v_mfma_f32_16x16x32_bf16 v[84:87], v[100:103], v[204:207], v[84:87]
	s_setprio 0
	s_setprio 1
	v_mfma_f32_16x16x32_bf16 v[136:139], v[120:123], v[172:175], v[136:139]
	v_mfma_f32_16x16x32_bf16 v[132:135], v[152:155], v[172:175], v[132:135]
	v_mfma_f32_16x16x32_bf16 v[116:119], v[120:123], v[180:183], v[116:119]
	v_mfma_f32_16x16x32_bf16 v[112:115], v[152:155], v[180:183], v[112:115]
	v_mfma_f32_16x16x32_bf16 v[96:99], v[120:123], v[192:195], v[96:99]
	v_mfma_f32_16x16x32_bf16 v[92:95], v[152:155], v[192:195], v[92:95]
	v_mfma_f32_16x16x32_bf16 v[76:79], v[120:123], v[200:203], v[76:79]
	v_mfma_f32_16x16x32_bf16 v[72:75], v[152:155], v[200:203], v[72:75]
	v_mfma_f32_16x16x32_bf16 v[136:139], v[140:143], v[176:179], v[136:139]
	v_mfma_f32_16x16x32_bf16 v[132:135], v[156:159], v[176:179], v[132:135]
	v_mfma_f32_16x16x32_bf16 v[116:119], v[140:143], v[184:187], v[116:119]
	v_mfma_f32_16x16x32_bf16 v[112:115], v[156:159], v[184:187], v[112:115]
	v_mfma_f32_16x16x32_bf16 v[96:99], v[140:143], v[196:199], v[96:99]
	v_mfma_f32_16x16x32_bf16 v[92:95], v[156:159], v[196:199], v[92:95]
	v_mfma_f32_16x16x32_bf16 v[76:79], v[140:143], v[204:207], v[76:79]
	v_mfma_f32_16x16x32_bf16 v[72:75], v[156:159], v[204:207], v[72:75]
	s_setprio 0
	s_barrier
	s_mov_b32 m0, s23
	v_lshl_add_u64 v[188:189], s[24:25], 0, v[162:163]
	s_add_u32 s30, s24, 0x4000
	ds_read_b128 v[172:175], v191 offset:16384
	ds_read_b128 v[176:179], v191 offset:17408
	ds_read_b128 v[180:183], v191 offset:18432
	ds_read_b128 v[184:187], v191 offset:19456
	ds_read_b128 v[192:195], v191 offset:20480
	ds_read_b128 v[196:199], v191 offset:21504
	ds_read_b128 v[200:203], v191 offset:22528
	ds_read_b128 v[204:207], v191 offset:23552
	global_load_lds_dwordx4 v[188:189], off
	v_lshl_add_u64 v[188:189], s[24:25], 0, v[166:167]
	s_mov_b32 m0, s74
	s_addc_u32 s31, s25, 0
	global_load_lds_dwordx4 v[188:189], off
	v_lshl_add_u64 v[188:189], s[30:31], 0, v[162:163]
	s_mov_b32 m0, s76
	v_lshl_add_u64 v[208:209], s[38:39], 0, v[164:165]
	global_load_lds_dwordx4 v[188:189], off
	v_lshl_add_u64 v[188:189], s[30:31], 0, v[166:167]
	s_mov_b32 m0, s77
	s_nop 0
	global_load_lds_dwordx4 v[188:189], off
	v_lshl_add_u64 v[188:189], s[38:39], 0, v[160:161]
	s_mov_b32 m0, s78
	s_nop 0
	global_load_lds_dwordx4 v[188:189], off
	s_mov_b32 m0, s79
	s_nop 0
	global_load_lds_dwordx4 v[208:209], off
	s_waitcnt vmcnt(8)
	s_waitcnt lgkmcnt(0)
	s_setprio 1
	s_barrier
	v_mfma_f32_16x16x32_bf16 v[68:71], v[40:43], v[172:175], v[68:71]
	v_mfma_f32_16x16x32_bf16 v[64:67], v[80:83], v[172:175], v[64:67]
	v_mfma_f32_16x16x32_bf16 v[48:51], v[40:43], v[180:183], v[48:51]
	v_mfma_f32_16x16x32_bf16 v[44:47], v[80:83], v[180:183], v[44:47]
	v_mfma_f32_16x16x32_bf16 v[28:31], v[40:43], v[192:195], v[28:31]
	v_mfma_f32_16x16x32_bf16 v[24:27], v[80:83], v[192:195], v[24:27]
	v_mfma_f32_16x16x32_bf16 v[12:15], v[40:43], v[200:203], v[12:15]
	v_mfma_f32_16x16x32_bf16 v[8:11], v[80:83], v[200:203], v[8:11]
	v_mfma_f32_16x16x32_bf16 v[68:71], v[60:63], v[176:179], v[68:71]
	v_mfma_f32_16x16x32_bf16 v[64:67], v[100:103], v[176:179], v[64:67]
	v_mfma_f32_16x16x32_bf16 v[48:51], v[60:63], v[184:187], v[48:51]
	v_mfma_f32_16x16x32_bf16 v[44:47], v[100:103], v[184:187], v[44:47]
	v_mfma_f32_16x16x32_bf16 v[28:31], v[60:63], v[196:199], v[28:31]
	v_mfma_f32_16x16x32_bf16 v[24:27], v[100:103], v[196:199], v[24:27]
	v_mfma_f32_16x16x32_bf16 v[12:15], v[60:63], v[204:207], v[12:15]
	v_mfma_f32_16x16x32_bf16 v[8:11], v[100:103], v[204:207], v[8:11]
	s_setprio 0
	s_setprio 1
	v_mfma_f32_16x16x32_bf16 v[52:55], v[152:155], v[172:175], v[52:55]
	v_mfma_f32_16x16x32_bf16 v[36:39], v[120:123], v[180:183], v[36:39]
	v_mfma_f32_16x16x32_bf16 v[32:35], v[152:155], v[180:183], v[32:35]
	v_mfma_f32_16x16x32_bf16 v[20:23], v[120:123], v[192:195], v[20:23]
	v_mfma_f32_16x16x32_bf16 v[16:19], v[152:155], v[192:195], v[16:19]
	v_mfma_f32_16x16x32_bf16 v[4:7], v[120:123], v[200:203], v[4:7]
	v_mfma_f32_16x16x32_bf16 v[0:3], v[152:155], v[200:203], v[0:3]
	v_mfma_f32_16x16x32_bf16 v[40:43], v[120:123], v[172:175], v[56:59]
	v_mfma_f32_16x16x32_bf16 v[52:55], v[156:159], v[176:179], v[52:55]
	v_mfma_f32_16x16x32_bf16 v[36:39], v[140:143], v[184:187], v[36:39]
	v_mfma_f32_16x16x32_bf16 v[32:35], v[156:159], v[184:187], v[32:35]
	v_mfma_f32_16x16x32_bf16 v[20:23], v[140:143], v[196:199], v[20:23]
	v_mfma_f32_16x16x32_bf16 v[16:19], v[156:159], v[196:199], v[16:19]
	v_mfma_f32_16x16x32_bf16 v[4:7], v[140:143], v[204:207], v[4:7]
	v_mfma_f32_16x16x32_bf16 v[0:3], v[156:159], v[204:207], v[0:3]
	v_mfma_f32_16x16x32_bf16 v[40:43], v[140:143], v[176:179], v[40:43]
	s_setprio 0
	s_barrier
	v_add_u32_e32 v100, s86, v190
	v_add_u32_e32 v156, s95, v190
	ds_read_b128 v[56:59], v100
	ds_read_b128 v[60:63], v100 offset:1024
	ds_read_b128 v[80:83], v100 offset:2048
	ds_read_b128 v[100:103], v100 offset:3072
	ds_read_b128 v[120:123], v156
	ds_read_b128 v[140:143], v156 offset:1024
	ds_read_b128 v[152:155], v156 offset:2048
	ds_read_b128 v[156:159], v156 offset:3072
	s_add_u32 s30, s38, 0x80000
	s_addc_u32 s31, s39, 0
	s_mov_b32 m0, s82
	v_lshl_add_u64 v[210:211], s[30:31], 0, v[160:161]
	ds_read_b128 v[172:175], v191 offset:32768
	ds_read_b128 v[176:179], v191 offset:33792
	ds_read_b128 v[180:183], v191 offset:34816
	ds_read_b128 v[184:187], v191 offset:35840
	ds_read_b128 v[192:195], v191 offset:36864
	ds_read_b128 v[196:199], v191 offset:37888
	ds_read_b128 v[200:203], v191 offset:38912
	ds_read_b128 v[204:207], v191 offset:39936
	global_load_lds_dwordx4 v[210:211], off
	v_lshl_add_u64 v[210:211], s[30:31], 0, v[164:165]
	s_mov_b32 m0, s83
	s_nop 0
	global_load_lds_dwordx4 v[210:211], off
	s_waitcnt vmcnt(8)
	s_waitcnt lgkmcnt(0)
	s_setprio 1
	s_barrier
	v_mfma_f32_16x16x32_bf16 v[148:151], v[56:59], v[172:175], v[148:151]
	v_mfma_f32_16x16x32_bf16 v[144:147], v[80:83], v[172:175], v[144:147]
	v_mfma_f32_16x16x32_bf16 v[128:131], v[56:59], v[180:183], v[128:131]
	v_mfma_f32_16x16x32_bf16 v[124:127], v[80:83], v[180:183], v[124:127]
	v_mfma_f32_16x16x32_bf16 v[108:111], v[56:59], v[192:195], v[108:111]
	v_mfma_f32_16x16x32_bf16 v[104:107], v[80:83], v[192:195], v[104:107]
	v_mfma_f32_16x16x32_bf16 v[88:91], v[56:59], v[200:203], v[88:91]
	v_mfma_f32_16x16x32_bf16 v[84:87], v[80:83], v[200:203], v[84:87]
	v_mfma_f32_16x16x32_bf16 v[148:151], v[60:63], v[176:179], v[148:151]
	v_mfma_f32_16x16x32_bf16 v[144:147], v[100:103], v[176:179], v[144:147]
	v_mfma_f32_16x16x32_bf16 v[128:131], v[60:63], v[184:187], v[128:131]
	v_mfma_f32_16x16x32_bf16 v[124:127], v[100:103], v[184:187], v[124:127]
	v_mfma_f32_16x16x32_bf16 v[108:111], v[60:63], v[196:199], v[108:111]
	v_mfma_f32_16x16x32_bf16 v[104:107], v[100:103], v[196:199], v[104:107]
	v_mfma_f32_16x16x32_bf16 v[88:91], v[60:63], v[204:207], v[88:91]
	v_mfma_f32_16x16x32_bf16 v[84:87], v[100:103], v[204:207], v[84:87]
	s_setprio 0
	s_setprio 1
	v_mfma_f32_16x16x32_bf16 v[136:139], v[120:123], v[172:175], v[136:139]
	v_mfma_f32_16x16x32_bf16 v[132:135], v[152:155], v[172:175], v[132:135]
	v_mfma_f32_16x16x32_bf16 v[116:119], v[120:123], v[180:183], v[116:119]
	v_mfma_f32_16x16x32_bf16 v[112:115], v[152:155], v[180:183], v[112:115]
	v_mfma_f32_16x16x32_bf16 v[96:99], v[120:123], v[192:195], v[96:99]
	v_mfma_f32_16x16x32_bf16 v[92:95], v[152:155], v[192:195], v[92:95]
	v_mfma_f32_16x16x32_bf16 v[76:79], v[120:123], v[200:203], v[76:79]
	v_mfma_f32_16x16x32_bf16 v[72:75], v[152:155], v[200:203], v[72:75]
	v_mfma_f32_16x16x32_bf16 v[136:139], v[140:143], v[176:179], v[136:139]
	v_mfma_f32_16x16x32_bf16 v[132:135], v[156:159], v[176:179], v[132:135]
	v_mfma_f32_16x16x32_bf16 v[116:119], v[140:143], v[184:187], v[116:119]
	v_mfma_f32_16x16x32_bf16 v[112:115], v[156:159], v[184:187], v[112:115]
	v_mfma_f32_16x16x32_bf16 v[96:99], v[140:143], v[196:199], v[96:99]
	v_mfma_f32_16x16x32_bf16 v[92:95], v[156:159], v[196:199], v[92:95]
	v_mfma_f32_16x16x32_bf16 v[76:79], v[140:143], v[204:207], v[76:79]
	v_mfma_f32_16x16x32_bf16 v[72:75], v[156:159], v[204:207], v[72:75]
	s_setprio 0
	s_barrier
	s_add_u32 s30, s24, 0x8000
	s_addc_u32 s31, s25, 0
	s_mov_b32 m0, s87
	v_lshl_add_u64 v[210:211], s[30:31], 0, v[162:163]
	s_add_u32 s24, s24, 0xc000
	ds_read_b128 v[172:175], v191 offset:49152
	ds_read_b128 v[176:179], v191 offset:50176
	ds_read_b128 v[180:183], v191 offset:51200
	ds_read_b128 v[184:187], v191 offset:52224
	ds_read_b128 v[192:195], v191 offset:53248
	ds_read_b128 v[196:199], v191 offset:54272
	ds_read_b128 v[200:203], v191 offset:55296
	ds_read_b128 v[204:207], v191 offset:56320
	global_load_lds_dwordx4 v[210:211], off
	v_lshl_add_u64 v[210:211], s[30:31], 0, v[166:167]
	s_mov_b32 m0, s92
	s_addc_u32 s25, s25, 0
	global_load_lds_dwordx4 v[210:211], off
	v_lshl_add_u64 v[210:211], s[24:25], 0, v[162:163]
	s_mov_b32 m0, s96
	v_lshl_add_u64 v[188:189], v[188:189], 0, s[26:27]
	global_load_lds_dwordx4 v[210:211], off
	v_lshl_add_u64 v[210:211], s[24:25], 0, v[166:167]
	s_mov_b32 m0, s97
	s_nop 0
	global_load_lds_dwordx4 v[210:211], off
	s_mov_b32 m0, s93
	s_nop 0
	global_load_lds_dwordx4 v[188:189], off
	v_lshl_add_u64 v[188:189], v[208:209], 0, s[26:27]
	s_mov_b32 m0, s94
	s_nop 0
	global_load_lds_dwordx4 v[188:189], off
	s_waitcnt vmcnt(8)
	s_waitcnt lgkmcnt(0)
	s_setprio 1
	s_barrier
	v_mfma_f32_16x16x32_bf16 v[68:71], v[56:59], v[172:175], v[68:71]
	v_mfma_f32_16x16x32_bf16 v[64:67], v[80:83], v[172:175], v[64:67]
	v_mfma_f32_16x16x32_bf16 v[48:51], v[56:59], v[180:183], v[48:51]
	v_mfma_f32_16x16x32_bf16 v[44:47], v[80:83], v[180:183], v[44:47]
	v_mfma_f32_16x16x32_bf16 v[28:31], v[56:59], v[192:195], v[28:31]
	v_mfma_f32_16x16x32_bf16 v[24:27], v[80:83], v[192:195], v[24:27]
	v_mfma_f32_16x16x32_bf16 v[12:15], v[56:59], v[200:203], v[12:15]
	v_mfma_f32_16x16x32_bf16 v[8:11], v[80:83], v[200:203], v[8:11]
	v_mfma_f32_16x16x32_bf16 v[68:71], v[60:63], v[176:179], v[68:71]
	v_mfma_f32_16x16x32_bf16 v[64:67], v[100:103], v[176:179], v[64:67]
	v_mfma_f32_16x16x32_bf16 v[48:51], v[60:63], v[184:187], v[48:51]
	v_mfma_f32_16x16x32_bf16 v[44:47], v[100:103], v[184:187], v[44:47]
	v_mfma_f32_16x16x32_bf16 v[28:31], v[60:63], v[196:199], v[28:31]
	v_mfma_f32_16x16x32_bf16 v[24:27], v[100:103], v[196:199], v[24:27]
	v_mfma_f32_16x16x32_bf16 v[12:15], v[60:63], v[204:207], v[12:15]
	v_mfma_f32_16x16x32_bf16 v[8:11], v[100:103], v[204:207], v[8:11]
	s_setprio 0
	s_setprio 1
	v_mfma_f32_16x16x32_bf16 v[40:43], v[120:123], v[172:175], v[40:43]
	v_mfma_f32_16x16x32_bf16 v[56:59], v[140:143], v[176:179], v[40:43]
	v_mfma_f32_16x16x32_bf16 v[40:43], v[152:155], v[172:175], v[52:55]
	v_mfma_f32_16x16x32_bf16 v[36:39], v[120:123], v[180:183], v[36:39]
	v_mfma_f32_16x16x32_bf16 v[32:35], v[152:155], v[180:183], v[32:35]
	v_mfma_f32_16x16x32_bf16 v[20:23], v[120:123], v[192:195], v[20:23]
	v_mfma_f32_16x16x32_bf16 v[16:19], v[152:155], v[192:195], v[16:19]
	v_mfma_f32_16x16x32_bf16 v[4:7], v[120:123], v[200:203], v[4:7]
	v_mfma_f32_16x16x32_bf16 v[0:3], v[152:155], v[200:203], v[0:3]
	v_mfma_f32_16x16x32_bf16 v[52:55], v[156:159], v[176:179], v[40:43]
	v_mfma_f32_16x16x32_bf16 v[36:39], v[140:143], v[184:187], v[36:39]
	v_mfma_f32_16x16x32_bf16 v[32:35], v[156:159], v[184:187], v[32:35]
	v_mfma_f32_16x16x32_bf16 v[20:23], v[140:143], v[196:199], v[20:23]
	v_mfma_f32_16x16x32_bf16 v[16:19], v[156:159], v[196:199], v[16:19]
	v_mfma_f32_16x16x32_bf16 v[4:7], v[140:143], v[204:207], v[4:7]
	v_mfma_f32_16x16x32_bf16 v[0:3], v[156:159], v[204:207], v[0:3]
	s_setprio 0
	s_barrier
	s_add_i32 s28, s28, 2
	s_add_u32 s17, s17, 0x10000
	s_addc_u32 s19, s19, 0
	s_add_u32 s0, s0, 0x100
	s_addc_u32 s1, s1, 0
	s_cmp_gt_u32 s28, 29
	s_cbranch_scc0 .LBB0_311
	s_and_b64 vcc, exec, s[34:35]
	s_cbranch_vccz .LBB0_314
	s_barrier

.LBB0_1054:
	s_ashr_i32 s41, s40, 31
	s_lshl_b64 s[4:5], s[40:41], 20
	s_add_u32 s44, s16, s4
	s_addc_u32 s45, s17, s5
	s_and_b64 s[4:5], s[36:37], exec
	s_cselect_b32 s4, s45, s51
	s_cselect_b32 s5, s44, s50
	s_ashr_i32 s39, s38, 31
	s_lshl_b64 s[46:47], s[38:39], 20
	s_add_u32 s46, s18, s46
	s_addc_u32 s47, s19, s47
	s_and_b64 s[52:53], s[36:37], exec
	s_cselect_b32 s39, s47, s1
	s_cselect_b32 s41, s46, s0
	s_add_u32 s49, s0, 0x10000
	s_addc_u32 s55, s1, 0
	s_add_u32 s0, s50, 0x80080
	s_addc_u32 s1, s51, 0
	s_mov_b32 s80, -2
	v_add_u32_e32 v140, s28, v215
	v_add_u32_e32 v156, s54, v215
	ds_read_b128 v[128:131], v140
	ds_read_b128 v[132:135], v140 offset:1024
	ds_read_b128 v[136:139], v140 offset:2048
	ds_read_b128 v[140:143], v140 offset:3072
	ds_read_b128 v[144:147], v156
	ds_read_b128 v[148:151], v156 offset:1024
	ds_read_b128 v[152:155], v156 offset:2048
	ds_read_b128 v[156:159], v156 offset:3072
	s_add_u32 s50, s0, 0xfff80080
	s_addc_u32 s51, s1, -1
	s_cmp_eq_u32 s80, 28
	s_cselect_b32 s53, s4, s51
	s_cselect_b32 s52, s5, s50
	s_cselect_b32 s51, s39, s55
	s_cselect_b32 s50, s41, s49
	v_lshl_add_u64 v[204:205], s[0:1], 0, v[180:181]
	s_add_i32 m0, s58, 0xc000
	ds_read_b128 v[160:163], v251
	ds_read_b128 v[164:167], v251 offset:1024
	ds_read_b128 v[168:171], v251 offset:2048
	ds_read_b128 v[184:187], v251 offset:3072
	ds_read_b128 v[188:191], v251 offset:4096
	ds_read_b128 v[192:195], v251 offset:5120
	ds_read_b128 v[196:199], v251 offset:6144
	ds_read_b128 v[200:203], v251 offset:7168
	global_load_lds_dwordx4 v[204:205], off
	v_lshl_add_u64 v[204:205], s[0:1], 0, v[182:183]
	s_add_i32 m0, s58, 0xe000
	s_nop 0
	global_load_lds_dwordx4 v[204:205], off
	s_waitcnt vmcnt(8)
	s_waitcnt lgkmcnt(0)
	s_setprio 1
	s_barrier
	v_mfma_f32_16x16x32_bf16 v[124:127], v[128:131], v[160:163], 0
	v_mfma_f32_16x16x32_bf16 v[120:123], v[136:139], v[160:163], 0
	v_mfma_f32_16x16x32_bf16 v[116:119], v[128:131], v[168:171], 0
	v_mfma_f32_16x16x32_bf16 v[112:115], v[136:139], v[168:171], 0
	v_mfma_f32_16x16x32_bf16 v[108:111], v[128:131], v[188:191], 0
	v_mfma_f32_16x16x32_bf16 v[104:107], v[136:139], v[188:191], 0
	v_mfma_f32_16x16x32_bf16 v[100:103], v[128:131], v[196:199], 0
	v_mfma_f32_16x16x32_bf16 v[96:99], v[136:139], v[196:199], 0
	v_mfma_f32_16x16x32_bf16 v[124:127], v[132:135], v[164:167], v[124:127]
	v_mfma_f32_16x16x32_bf16 v[120:123], v[140:143], v[164:167], v[120:123]
	v_mfma_f32_16x16x32_bf16 v[116:119], v[132:135], v[184:187], v[116:119]
	v_mfma_f32_16x16x32_bf16 v[112:115], v[140:143], v[184:187], v[112:115]
	v_mfma_f32_16x16x32_bf16 v[108:111], v[132:135], v[192:195], v[108:111]
	v_mfma_f32_16x16x32_bf16 v[104:107], v[140:143], v[192:195], v[104:107]
	v_mfma_f32_16x16x32_bf16 v[100:103], v[132:135], v[200:203], v[100:103]
	v_mfma_f32_16x16x32_bf16 v[96:99], v[140:143], v[200:203], v[96:99]
	s_setprio 0
	s_setprio 1
	v_mfma_f32_16x16x32_bf16 v[60:63], v[144:147], v[160:163], 0
	v_mfma_f32_16x16x32_bf16 v[56:59], v[152:155], v[160:163], 0
	v_mfma_f32_16x16x32_bf16 v[52:55], v[144:147], v[168:171], 0
	v_mfma_f32_16x16x32_bf16 v[48:51], v[152:155], v[168:171], 0
	v_mfma_f32_16x16x32_bf16 v[44:47], v[144:147], v[188:191], 0
	v_mfma_f32_16x16x32_bf16 v[40:43], v[152:155], v[188:191], 0
	v_mfma_f32_16x16x32_bf16 v[36:39], v[144:147], v[196:199], 0
	v_mfma_f32_16x16x32_bf16 v[32:35], v[152:155], v[196:199], 0
	v_mfma_f32_16x16x32_bf16 v[60:63], v[148:151], v[164:167], v[60:63]
	v_mfma_f32_16x16x32_bf16 v[56:59], v[156:159], v[164:167], v[56:59]
	v_mfma_f32_16x16x32_bf16 v[52:55], v[148:151], v[184:187], v[52:55]
	v_mfma_f32_16x16x32_bf16 v[48:51], v[156:159], v[184:187], v[48:51]
	v_mfma_f32_16x16x32_bf16 v[44:47], v[148:151], v[192:195], v[44:47]
	v_mfma_f32_16x16x32_bf16 v[40:43], v[156:159], v[192:195], v[40:43]
	v_mfma_f32_16x16x32_bf16 v[36:39], v[148:151], v[200:203], v[36:39]
	v_mfma_f32_16x16x32_bf16 v[32:35], v[156:159], v[200:203], v[32:35]
	s_setprio 0
	s_barrier
	s_mov_b32 m0, s30
	v_lshl_add_u64 v[204:205], s[50:51], 0, v[174:175]
	s_add_u32 s82, s50, 0x4000
	ds_read_b128 v[160:163], v251 offset:16384
	ds_read_b128 v[164:167], v251 offset:17408
	ds_read_b128 v[168:171], v251 offset:18432
	ds_read_b128 v[184:187], v251 offset:19456
	ds_read_b128 v[188:191], v251 offset:20480
	ds_read_b128 v[192:195], v251 offset:21504
	ds_read_b128 v[196:199], v251 offset:22528
	ds_read_b128 v[200:203], v251 offset:23552
	global_load_lds_dwordx4 v[204:205], off
	v_lshl_add_u64 v[204:205], s[50:51], 0, v[178:179]
	s_mov_b32 m0, s43
	s_addc_u32 s83, s51, 0
	global_load_lds_dwordx4 v[204:205], off
	v_lshl_add_u64 v[204:205], s[82:83], 0, v[174:175]
	s_mov_b32 m0, s56
	v_lshl_add_u64 v[206:207], s[52:53], 0, v[176:177]
	global_load_lds_dwordx4 v[204:205], off
	v_lshl_add_u64 v[204:205], s[82:83], 0, v[178:179]
	s_mov_b32 m0, s57
	s_nop 0
	global_load_lds_dwordx4 v[204:205], off
	v_lshl_add_u64 v[204:205], s[52:53], 0, v[172:173]
	s_mov_b32 m0, s58
	s_nop 0
	global_load_lds_dwordx4 v[204:205], off
	s_mov_b32 m0, s59
	s_nop 0
	global_load_lds_dwordx4 v[206:207], off
	s_waitcnt vmcnt(8)
	s_waitcnt lgkmcnt(0)
	s_setprio 1
	s_barrier
	v_mfma_f32_16x16x32_bf16 v[92:95], v[128:131], v[160:163], 0
	v_mfma_f32_16x16x32_bf16 v[88:91], v[136:139], v[160:163], 0
	v_mfma_f32_16x16x32_bf16 v[84:87], v[128:131], v[168:171], 0
	v_mfma_f32_16x16x32_bf16 v[80:83], v[136:139], v[168:171], 0
	v_mfma_f32_16x16x32_bf16 v[76:79], v[128:131], v[188:191], 0
	v_mfma_f32_16x16x32_bf16 v[72:75], v[136:139], v[188:191], 0
	v_mfma_f32_16x16x32_bf16 v[68:71], v[128:131], v[196:199], 0
	v_mfma_f32_16x16x32_bf16 v[64:67], v[136:139], v[196:199], 0
	v_mfma_f32_16x16x32_bf16 v[92:95], v[132:135], v[164:167], v[92:95]
	v_mfma_f32_16x16x32_bf16 v[88:91], v[140:143], v[164:167], v[88:91]
	v_mfma_f32_16x16x32_bf16 v[84:87], v[132:135], v[184:187], v[84:87]
	v_mfma_f32_16x16x32_bf16 v[80:83], v[140:143], v[184:187], v[80:83]
	v_mfma_f32_16x16x32_bf16 v[76:79], v[132:135], v[192:195], v[76:79]
	v_mfma_f32_16x16x32_bf16 v[72:75], v[140:143], v[192:195], v[72:75]
	v_mfma_f32_16x16x32_bf16 v[68:71], v[132:135], v[200:203], v[68:71]
	v_mfma_f32_16x16x32_bf16 v[64:67], v[140:143], v[200:203], v[64:67]
	s_setprio 0
	s_setprio 1
	v_mfma_f32_16x16x32_bf16 v[28:31], v[144:147], v[160:163], 0
	v_mfma_f32_16x16x32_bf16 v[24:27], v[152:155], v[160:163], 0
	v_mfma_f32_16x16x32_bf16 v[20:23], v[144:147], v[168:171], 0
	v_mfma_f32_16x16x32_bf16 v[16:19], v[152:155], v[168:171], 0
	v_mfma_f32_16x16x32_bf16 v[12:15], v[144:147], v[188:191], 0
	v_mfma_f32_16x16x32_bf16 v[8:11], v[152:155], v[188:191], 0
	v_mfma_f32_16x16x32_bf16 v[4:7], v[144:147], v[196:199], 0
	v_mfma_f32_16x16x32_bf16 v[0:3], v[152:155], v[196:199], 0
	v_mfma_f32_16x16x32_bf16 v[28:31], v[148:151], v[164:167], v[28:31]
	v_mfma_f32_16x16x32_bf16 v[24:27], v[156:159], v[164:167], v[24:27]
	v_mfma_f32_16x16x32_bf16 v[20:23], v[148:151], v[184:187], v[20:23]
	v_mfma_f32_16x16x32_bf16 v[16:19], v[156:159], v[184:187], v[16:19]
	v_mfma_f32_16x16x32_bf16 v[12:15], v[148:151], v[192:195], v[12:15]
	v_mfma_f32_16x16x32_bf16 v[8:11], v[156:159], v[192:195], v[8:11]
	v_mfma_f32_16x16x32_bf16 v[4:7], v[148:151], v[200:203], v[4:7]
	v_mfma_f32_16x16x32_bf16 v[0:3], v[156:159], v[200:203], v[0:3]
	s_setprio 0
	s_barrier
	v_add_u32_e32 v140, s68, v215
	v_add_u32_e32 v156, s73, v215
	ds_read_b128 v[128:131], v140
	ds_read_b128 v[132:135], v140 offset:1024
	ds_read_b128 v[136:139], v140 offset:2048
	ds_read_b128 v[140:143], v140 offset:3072
	ds_read_b128 v[144:147], v156
	ds_read_b128 v[148:151], v156 offset:1024
	ds_read_b128 v[152:155], v156 offset:2048
	ds_read_b128 v[156:159], v156 offset:3072
	s_add_u32 s52, s52, 0x80000
	s_addc_u32 s53, s53, 0
	s_mov_b32 m0, s60
	v_lshl_add_u64 v[208:209], s[52:53], 0, v[172:173]
	ds_read_b128 v[160:163], v251 offset:32768
	ds_read_b128 v[164:167], v251 offset:33792
	ds_read_b128 v[168:171], v251 offset:34816
	ds_read_b128 v[184:187], v251 offset:35840
	ds_read_b128 v[188:191], v251 offset:36864
	ds_read_b128 v[192:195], v251 offset:37888
	ds_read_b128 v[196:199], v251 offset:38912
	ds_read_b128 v[200:203], v251 offset:39936
	global_load_lds_dwordx4 v[208:209], off
	v_lshl_add_u64 v[208:209], s[52:53], 0, v[176:177]
	s_mov_b32 m0, s61
	s_nop 0
	global_load_lds_dwordx4 v[208:209], off
	s_waitcnt vmcnt(8)
	s_waitcnt lgkmcnt(0)
	s_setprio 1
	s_barrier
	v_mfma_f32_16x16x32_bf16 v[124:127], v[128:131], v[160:163], v[124:127]
	v_mfma_f32_16x16x32_bf16 v[120:123], v[136:139], v[160:163], v[120:123]
	v_mfma_f32_16x16x32_bf16 v[116:119], v[128:131], v[168:171], v[116:119]
	v_mfma_f32_16x16x32_bf16 v[112:115], v[136:139], v[168:171], v[112:115]
	v_mfma_f32_16x16x32_bf16 v[108:111], v[128:131], v[188:191], v[108:111]
	v_mfma_f32_16x16x32_bf16 v[104:107], v[136:139], v[188:191], v[104:107]
	v_mfma_f32_16x16x32_bf16 v[100:103], v[128:131], v[196:199], v[100:103]
	v_mfma_f32_16x16x32_bf16 v[96:99], v[136:139], v[196:199], v[96:99]
	v_mfma_f32_16x16x32_bf16 v[124:127], v[132:135], v[164:167], v[124:127]
	v_mfma_f32_16x16x32_bf16 v[120:123], v[140:143], v[164:167], v[120:123]
	v_mfma_f32_16x16x32_bf16 v[116:119], v[132:135], v[184:187], v[116:119]
	v_mfma_f32_16x16x32_bf16 v[112:115], v[140:143], v[184:187], v[112:115]
	v_mfma_f32_16x16x32_bf16 v[108:111], v[132:135], v[192:195], v[108:111]
	v_mfma_f32_16x16x32_bf16 v[104:107], v[140:143], v[192:195], v[104:107]
	v_mfma_f32_16x16x32_bf16 v[100:103], v[132:135], v[200:203], v[100:103]
	v_mfma_f32_16x16x32_bf16 v[96:99], v[140:143], v[200:203], v[96:99]
	s_setprio 0
	s_setprio 1
	v_mfma_f32_16x16x32_bf16 v[60:63], v[144:147], v[160:163], v[60:63]
	v_mfma_f32_16x16x32_bf16 v[56:59], v[152:155], v[160:163], v[56:59]
	v_mfma_f32_16x16x32_bf16 v[52:55], v[144:147], v[168:171], v[52:55]
	v_mfma_f32_16x16x32_bf16 v[48:51], v[152:155], v[168:171], v[48:51]
	v_mfma_f32_16x16x32_bf16 v[44:47], v[144:147], v[188:191], v[44:47]
	v_mfma_f32_16x16x32_bf16 v[40:43], v[152:155], v[188:191], v[40:43]
	v_mfma_f32_16x16x32_bf16 v[36:39], v[144:147], v[196:199], v[36:39]
	v_mfma_f32_16x16x32_bf16 v[32:35], v[152:155], v[196:199], v[32:35]
	v_mfma_f32_16x16x32_bf16 v[60:63], v[148:151], v[164:167], v[60:63]
	v_mfma_f32_16x16x32_bf16 v[56:59], v[156:159], v[164:167], v[56:59]
	v_mfma_f32_16x16x32_bf16 v[52:55], v[148:151], v[184:187], v[52:55]
	v_mfma_f32_16x16x32_bf16 v[48:51], v[156:159], v[184:187], v[48:51]
	v_mfma_f32_16x16x32_bf16 v[44:47], v[148:151], v[192:195], v[44:47]
	v_mfma_f32_16x16x32_bf16 v[40:43], v[156:159], v[192:195], v[40:43]
	v_mfma_f32_16x16x32_bf16 v[36:39], v[148:151], v[200:203], v[36:39]
	v_mfma_f32_16x16x32_bf16 v[32:35], v[156:159], v[200:203], v[32:35]
	s_setprio 0
	s_barrier
	s_add_u32 s52, s50, 0x8000
	s_addc_u32 s53, s51, 0
	s_mov_b32 m0, s69
	v_lshl_add_u64 v[208:209], s[52:53], 0, v[174:175]
	s_add_u32 s50, s50, 0xc000
	ds_read_b128 v[160:163], v251 offset:49152
	ds_read_b128 v[164:167], v251 offset:50176
	ds_read_b128 v[168:171], v251 offset:51200
	ds_read_b128 v[184:187], v251 offset:52224
	ds_read_b128 v[188:191], v251 offset:53248
	ds_read_b128 v[192:195], v251 offset:54272
	ds_read_b128 v[196:199], v251 offset:55296
	ds_read_b128 v[200:203], v251 offset:56320
	global_load_lds_dwordx4 v[208:209], off
	v_lshl_add_u64 v[208:209], s[52:53], 0, v[178:179]
	s_mov_b32 m0, s70
	s_addc_u32 s51, s51, 0
	global_load_lds_dwordx4 v[208:209], off
	v_lshl_add_u64 v[208:209], s[50:51], 0, v[174:175]
	s_mov_b32 m0, s74
	v_lshl_add_u64 v[204:205], v[204:205], 0, s[26:27]
	global_load_lds_dwordx4 v[208:209], off
	v_lshl_add_u64 v[208:209], s[50:51], 0, v[178:179]
	s_mov_b32 m0, s75
	s_nop 0
	global_load_lds_dwordx4 v[208:209], off
	s_mov_b32 m0, s71
	s_nop 0
	global_load_lds_dwordx4 v[204:205], off
	v_lshl_add_u64 v[204:205], v[206:207], 0, s[26:27]
	s_mov_b32 m0, s72
	s_nop 0
	global_load_lds_dwordx4 v[204:205], off
	s_waitcnt vmcnt(8)
	s_waitcnt lgkmcnt(0)
	s_setprio 1
	s_barrier
	v_mfma_f32_16x16x32_bf16 v[92:95], v[128:131], v[160:163], v[92:95]
	v_mfma_f32_16x16x32_bf16 v[88:91], v[136:139], v[160:163], v[88:91]
	v_mfma_f32_16x16x32_bf16 v[84:87], v[128:131], v[168:171], v[84:87]
	v_mfma_f32_16x16x32_bf16 v[80:83], v[136:139], v[168:171], v[80:83]
	v_mfma_f32_16x16x32_bf16 v[76:79], v[128:131], v[188:191], v[76:79]
	v_mfma_f32_16x16x32_bf16 v[72:75], v[136:139], v[188:191], v[72:75]
	v_mfma_f32_16x16x32_bf16 v[68:71], v[128:131], v[196:199], v[68:71]
	v_mfma_f32_16x16x32_bf16 v[64:67], v[136:139], v[196:199], v[64:67]
	v_mfma_f32_16x16x32_bf16 v[92:95], v[132:135], v[164:167], v[92:95]
	v_mfma_f32_16x16x32_bf16 v[88:91], v[140:143], v[164:167], v[88:91]
	v_mfma_f32_16x16x32_bf16 v[84:87], v[132:135], v[184:187], v[84:87]
	v_mfma_f32_16x16x32_bf16 v[80:83], v[140:143], v[184:187], v[80:83]
	v_mfma_f32_16x16x32_bf16 v[76:79], v[132:135], v[192:195], v[76:79]
	v_mfma_f32_16x16x32_bf16 v[72:75], v[140:143], v[192:195], v[72:75]
	v_mfma_f32_16x16x32_bf16 v[68:71], v[132:135], v[200:203], v[68:71]
	v_mfma_f32_16x16x32_bf16 v[64:67], v[140:143], v[200:203], v[64:67]
	s_setprio 0
	s_setprio 1
	v_mfma_f32_16x16x32_bf16 v[28:31], v[144:147], v[160:163], v[28:31]
	v_mfma_f32_16x16x32_bf16 v[24:27], v[152:155], v[160:163], v[24:27]
	v_mfma_f32_16x16x32_bf16 v[20:23], v[144:147], v[168:171], v[20:23]
	v_mfma_f32_16x16x32_bf16 v[16:19], v[152:155], v[168:171], v[16:19]
	v_mfma_f32_16x16x32_bf16 v[12:15], v[144:147], v[188:191], v[12:15]
	v_mfma_f32_16x16x32_bf16 v[8:11], v[152:155], v[188:191], v[8:11]
	v_mfma_f32_16x16x32_bf16 v[4:7], v[144:147], v[196:199], v[4:7]
	v_mfma_f32_16x16x32_bf16 v[0:3], v[152:155], v[196:199], v[0:3]
	v_mfma_f32_16x16x32_bf16 v[28:31], v[148:151], v[164:167], v[28:31]
	v_mfma_f32_16x16x32_bf16 v[24:27], v[156:159], v[164:167], v[24:27]
	v_mfma_f32_16x16x32_bf16 v[20:23], v[148:151], v[184:187], v[20:23]
	v_mfma_f32_16x16x32_bf16 v[16:19], v[156:159], v[184:187], v[16:19]
	v_mfma_f32_16x16x32_bf16 v[12:15], v[148:151], v[192:195], v[12:15]
	v_mfma_f32_16x16x32_bf16 v[8:11], v[156:159], v[192:195], v[8:11]
	v_mfma_f32_16x16x32_bf16 v[4:7], v[148:151], v[200:203], v[4:7]
	v_mfma_f32_16x16x32_bf16 v[0:3], v[156:159], v[200:203], v[0:3]
	s_setprio 0
	s_barrier
	s_add_i32 s80, s80, 2
	s_add_u32 s49, s49, 0x10000
	s_addc_u32 s55, s55, 0
	s_add_u32 s0, s0, 0x100
	s_addc_u32 s1, s1, 0
	s_cmp_gt_u32 s80, 29
.LBB0_1055:
	v_add_u32_e32 v140, s28, v215
	v_add_u32_e32 v156, s54, v215
	ds_read_b128 v[128:131], v140
	ds_read_b128 v[132:135], v140 offset:1024
	ds_read_b128 v[136:139], v140 offset:2048
	ds_read_b128 v[140:143], v140 offset:3072
	ds_read_b128 v[144:147], v156
	ds_read_b128 v[148:151], v156 offset:1024
	ds_read_b128 v[152:155], v156 offset:2048
	ds_read_b128 v[156:159], v156 offset:3072
	s_add_u32 s50, s0, 0xfff80080
	s_addc_u32 s51, s1, -1
	s_cmp_eq_u32 s80, 28
	s_cselect_b32 s53, s4, s51
	s_cselect_b32 s52, s5, s50
	s_cselect_b32 s51, s39, s55
	s_cselect_b32 s50, s41, s49
	v_lshl_add_u64 v[204:205], s[0:1], 0, v[180:181]
	s_add_i32 m0, s58, 0xc000
	ds_read_b128 v[160:163], v251
	ds_read_b128 v[164:167], v251 offset:1024
	ds_read_b128 v[168:171], v251 offset:2048
	ds_read_b128 v[184:187], v251 offset:3072
	ds_read_b128 v[188:191], v251 offset:4096
	ds_read_b128 v[192:195], v251 offset:5120
	ds_read_b128 v[196:199], v251 offset:6144
	ds_read_b128 v[200:203], v251 offset:7168
	global_load_lds_dwordx4 v[204:205], off
	v_lshl_add_u64 v[204:205], s[0:1], 0, v[182:183]
	s_add_i32 m0, s58, 0xe000
	s_nop 0
	global_load_lds_dwordx4 v[204:205], off
	s_waitcnt vmcnt(8)
	s_waitcnt lgkmcnt(0)
	s_setprio 1
	s_barrier
	v_mfma_f32_16x16x32_bf16 v[124:127], v[128:131], v[160:163], v[124:127]
	v_mfma_f32_16x16x32_bf16 v[120:123], v[136:139], v[160:163], v[120:123]
	v_mfma_f32_16x16x32_bf16 v[116:119], v[128:131], v[168:171], v[116:119]
	v_mfma_f32_16x16x32_bf16 v[112:115], v[136:139], v[168:171], v[112:115]
	v_mfma_f32_16x16x32_bf16 v[108:111], v[128:131], v[188:191], v[108:111]
	v_mfma_f32_16x16x32_bf16 v[104:107], v[136:139], v[188:191], v[104:107]
	v_mfma_f32_16x16x32_bf16 v[100:103], v[128:131], v[196:199], v[100:103]
	v_mfma_f32_16x16x32_bf16 v[96:99], v[136:139], v[196:199], v[96:99]
	v_mfma_f32_16x16x32_bf16 v[124:127], v[132:135], v[164:167], v[124:127]
	v_mfma_f32_16x16x32_bf16 v[120:123], v[140:143], v[164:167], v[120:123]
	v_mfma_f32_16x16x32_bf16 v[116:119], v[132:135], v[184:187], v[116:119]
	v_mfma_f32_16x16x32_bf16 v[112:115], v[140:143], v[184:187], v[112:115]
	v_mfma_f32_16x16x32_bf16 v[108:111], v[132:135], v[192:195], v[108:111]
	v_mfma_f32_16x16x32_bf16 v[104:107], v[140:143], v[192:195], v[104:107]
	v_mfma_f32_16x16x32_bf16 v[100:103], v[132:135], v[200:203], v[100:103]
	v_mfma_f32_16x16x32_bf16 v[96:99], v[140:143], v[200:203], v[96:99]
	s_setprio 0
	s_setprio 1
	v_mfma_f32_16x16x32_bf16 v[60:63], v[144:147], v[160:163], v[60:63]
	v_mfma_f32_16x16x32_bf16 v[56:59], v[152:155], v[160:163], v[56:59]
	v_mfma_f32_16x16x32_bf16 v[52:55], v[144:147], v[168:171], v[52:55]
	v_mfma_f32_16x16x32_bf16 v[48:51], v[152:155], v[168:171], v[48:51]
	v_mfma_f32_16x16x32_bf16 v[44:47], v[144:147], v[188:191], v[44:47]
	v_mfma_f32_16x16x32_bf16 v[40:43], v[152:155], v[188:191], v[40:43]
	v_mfma_f32_16x16x32_bf16 v[36:39], v[144:147], v[196:199], v[36:39]
	v_mfma_f32_16x16x32_bf16 v[32:35], v[152:155], v[196:199], v[32:35]
	v_mfma_f32_16x16x32_bf16 v[60:63], v[148:151], v[164:167], v[60:63]
	v_mfma_f32_16x16x32_bf16 v[56:59], v[156:159], v[164:167], v[56:59]
	v_mfma_f32_16x16x32_bf16 v[52:55], v[148:151], v[184:187], v[52:55]
	v_mfma_f32_16x16x32_bf16 v[48:51], v[156:159], v[184:187], v[48:51]
	v_mfma_f32_16x16x32_bf16 v[44:47], v[148:151], v[192:195], v[44:47]
	v_mfma_f32_16x16x32_bf16 v[40:43], v[156:159], v[192:195], v[40:43]
	v_mfma_f32_16x16x32_bf16 v[36:39], v[148:151], v[200:203], v[36:39]
	v_mfma_f32_16x16x32_bf16 v[32:35], v[156:159], v[200:203], v[32:35]
	s_setprio 0
	s_barrier
	s_mov_b32 m0, s30
	v_lshl_add_u64 v[204:205], s[50:51], 0, v[174:175]
	s_add_u32 s82, s50, 0x4000
	ds_read_b128 v[160:163], v251 offset:16384
	ds_read_b128 v[164:167], v251 offset:17408
	ds_read_b128 v[168:171], v251 offset:18432
	ds_read_b128 v[184:187], v251 offset:19456
	ds_read_b128 v[188:191], v251 offset:20480
	ds_read_b128 v[192:195], v251 offset:21504
	ds_read_b128 v[196:199], v251 offset:22528
	ds_read_b128 v[200:203], v251 offset:23552
	global_load_lds_dwordx4 v[204:205], off
	v_lshl_add_u64 v[204:205], s[50:51], 0, v[178:179]
	s_mov_b32 m0, s43
	s_addc_u32 s83, s51, 0
	global_load_lds_dwordx4 v[204:205], off
	v_lshl_add_u64 v[204:205], s[82:83], 0, v[174:175]
	s_mov_b32 m0, s56
	v_lshl_add_u64 v[206:207], s[52:53], 0, v[176:177]
	global_load_lds_dwordx4 v[204:205], off
	v_lshl_add_u64 v[204:205], s[82:83], 0, v[178:179]
	s_mov_b32 m0, s57
	s_nop 0
	global_load_lds_dwordx4 v[204:205], off
	v_lshl_add_u64 v[204:205], s[52:53], 0, v[172:173]
	s_mov_b32 m0, s58
	s_nop 0
	global_load_lds_dwordx4 v[204:205], off
	s_mov_b32 m0, s59
	s_nop 0
	global_load_lds_dwordx4 v[206:207], off
	s_waitcnt vmcnt(8)
	s_waitcnt lgkmcnt(0)
	s_setprio 1
	s_barrier
	v_mfma_f32_16x16x32_bf16 v[92:95], v[128:131], v[160:163], v[92:95]
	v_mfma_f32_16x16x32_bf16 v[88:91], v[136:139], v[160:163], v[88:91]
	v_mfma_f32_16x16x32_bf16 v[84:87], v[128:131], v[168:171], v[84:87]
	v_mfma_f32_16x16x32_bf16 v[80:83], v[136:139], v[168:171], v[80:83]
	v_mfma_f32_16x16x32_bf16 v[76:79], v[128:131], v[188:191], v[76:79]
	v_mfma_f32_16x16x32_bf16 v[72:75], v[136:139], v[188:191], v[72:75]
	v_mfma_f32_16x16x32_bf16 v[68:71], v[128:131], v[196:199], v[68:71]
	v_mfma_f32_16x16x32_bf16 v[64:67], v[136:139], v[196:199], v[64:67]
	v_mfma_f32_16x16x32_bf16 v[92:95], v[132:135], v[164:167], v[92:95]
	v_mfma_f32_16x16x32_bf16 v[88:91], v[140:143], v[164:167], v[88:91]
	v_mfma_f32_16x16x32_bf16 v[84:87], v[132:135], v[184:187], v[84:87]
	v_mfma_f32_16x16x32_bf16 v[80:83], v[140:143], v[184:187], v[80:83]
	v_mfma_f32_16x16x32_bf16 v[76:79], v[132:135], v[192:195], v[76:79]
	v_mfma_f32_16x16x32_bf16 v[72:75], v[140:143], v[192:195], v[72:75]
	v_mfma_f32_16x16x32_bf16 v[68:71], v[132:135], v[200:203], v[68:71]
	v_mfma_f32_16x16x32_bf16 v[64:67], v[140:143], v[200:203], v[64:67]
	s_setprio 0
	s_setprio 1
	v_mfma_f32_16x16x32_bf16 v[28:31], v[144:147], v[160:163], v[28:31]
	v_mfma_f32_16x16x32_bf16 v[24:27], v[152:155], v[160:163], v[24:27]
	v_mfma_f32_16x16x32_bf16 v[20:23], v[144:147], v[168:171], v[20:23]
	v_mfma_f32_16x16x32_bf16 v[16:19], v[152:155], v[168:171], v[16:19]
	v_mfma_f32_16x16x32_bf16 v[12:15], v[144:147], v[188:191], v[12:15]
	v_mfma_f32_16x16x32_bf16 v[8:11], v[152:155], v[188:191], v[8:11]
	v_mfma_f32_16x16x32_bf16 v[4:7], v[144:147], v[196:199], v[4:7]
	v_mfma_f32_16x16x32_bf16 v[0:3], v[152:155], v[196:199], v[0:3]
	v_mfma_f32_16x16x32_bf16 v[28:31], v[148:151], v[164:167], v[28:31]
	v_mfma_f32_16x16x32_bf16 v[24:27], v[156:159], v[164:167], v[24:27]
	v_mfma_f32_16x16x32_bf16 v[20:23], v[148:151], v[184:187], v[20:23]
	v_mfma_f32_16x16x32_bf16 v[16:19], v[156:159], v[184:187], v[16:19]
	v_mfma_f32_16x16x32_bf16 v[12:15], v[148:151], v[192:195], v[12:15]
	v_mfma_f32_16x16x32_bf16 v[8:11], v[156:159], v[192:195], v[8:11]
	v_mfma_f32_16x16x32_bf16 v[4:7], v[148:151], v[200:203], v[4:7]
	v_mfma_f32_16x16x32_bf16 v[0:3], v[156:159], v[200:203], v[0:3]
	s_setprio 0
	s_barrier
	v_add_u32_e32 v140, s68, v215
	v_add_u32_e32 v156, s73, v215
	ds_read_b128 v[128:131], v140
	ds_read_b128 v[132:135], v140 offset:1024
	ds_read_b128 v[136:139], v140 offset:2048
	ds_read_b128 v[140:143], v140 offset:3072
	ds_read_b128 v[144:147], v156
	ds_read_b128 v[148:151], v156 offset:1024
	ds_read_b128 v[152:155], v156 offset:2048
	ds_read_b128 v[156:159], v156 offset:3072
	s_add_u32 s52, s52, 0x80000
	s_addc_u32 s53, s53, 0
	s_mov_b32 m0, s60
	v_lshl_add_u64 v[208:209], s[52:53], 0, v[172:173]
	ds_read_b128 v[160:163], v251 offset:32768
	ds_read_b128 v[164:167], v251 offset:33792
	ds_read_b128 v[168:171], v251 offset:34816
	ds_read_b128 v[184:187], v251 offset:35840
	ds_read_b128 v[188:191], v251 offset:36864
	ds_read_b128 v[192:195], v251 offset:37888
	ds_read_b128 v[196:199], v251 offset:38912
	ds_read_b128 v[200:203], v251 offset:39936
	global_load_lds_dwordx4 v[208:209], off
	v_lshl_add_u64 v[208:209], s[52:53], 0, v[176:177]
	s_mov_b32 m0, s61
	s_nop 0
	global_load_lds_dwordx4 v[208:209], off
	s_waitcnt vmcnt(8)
	s_waitcnt lgkmcnt(0)
	s_setprio 1
	s_barrier
	v_mfma_f32_16x16x32_bf16 v[124:127], v[128:131], v[160:163], v[124:127]
	v_mfma_f32_16x16x32_bf16 v[120:123], v[136:139], v[160:163], v[120:123]
	v_mfma_f32_16x16x32_bf16 v[116:119], v[128:131], v[168:171], v[116:119]
	v_mfma_f32_16x16x32_bf16 v[112:115], v[136:139], v[168:171], v[112:115]
	v_mfma_f32_16x16x32_bf16 v[108:111], v[128:131], v[188:191], v[108:111]
	v_mfma_f32_16x16x32_bf16 v[104:107], v[136:139], v[188:191], v[104:107]
	v_mfma_f32_16x16x32_bf16 v[100:103], v[128:131], v[196:199], v[100:103]
	v_mfma_f32_16x16x32_bf16 v[96:99], v[136:139], v[196:199], v[96:99]
	v_mfma_f32_16x16x32_bf16 v[124:127], v[132:135], v[164:167], v[124:127]
	v_mfma_f32_16x16x32_bf16 v[120:123], v[140:143], v[164:167], v[120:123]
	v_mfma_f32_16x16x32_bf16 v[116:119], v[132:135], v[184:187], v[116:119]
	v_mfma_f32_16x16x32_bf16 v[112:115], v[140:143], v[184:187], v[112:115]
	v_mfma_f32_16x16x32_bf16 v[108:111], v[132:135], v[192:195], v[108:111]
	v_mfma_f32_16x16x32_bf16 v[104:107], v[140:143], v[192:195], v[104:107]
	v_mfma_f32_16x16x32_bf16 v[100:103], v[132:135], v[200:203], v[100:103]
	v_mfma_f32_16x16x32_bf16 v[96:99], v[140:143], v[200:203], v[96:99]
	s_setprio 0
	s_setprio 1
	v_mfma_f32_16x16x32_bf16 v[60:63], v[144:147], v[160:163], v[60:63]
	v_mfma_f32_16x16x32_bf16 v[56:59], v[152:155], v[160:163], v[56:59]
	v_mfma_f32_16x16x32_bf16 v[52:55], v[144:147], v[168:171], v[52:55]
	v_mfma_f32_16x16x32_bf16 v[48:51], v[152:155], v[168:171], v[48:51]
	v_mfma_f32_16x16x32_bf16 v[44:47], v[144:147], v[188:191], v[44:47]
	v_mfma_f32_16x16x32_bf16 v[40:43], v[152:155], v[188:191], v[40:43]
	v_mfma_f32_16x16x32_bf16 v[36:39], v[144:147], v[196:199], v[36:39]
	v_mfma_f32_16x16x32_bf16 v[32:35], v[152:155], v[196:199], v[32:35]
	v_mfma_f32_16x16x32_bf16 v[60:63], v[148:151], v[164:167], v[60:63]
	v_mfma_f32_16x16x32_bf16 v[56:59], v[156:159], v[164:167], v[56:59]
	v_mfma_f32_16x16x32_bf16 v[52:55], v[148:151], v[184:187], v[52:55]
	v_mfma_f32_16x16x32_bf16 v[48:51], v[156:159], v[184:187], v[48:51]
	v_mfma_f32_16x16x32_bf16 v[44:47], v[148:151], v[192:195], v[44:47]
	v_mfma_f32_16x16x32_bf16 v[40:43], v[156:159], v[192:195], v[40:43]
	v_mfma_f32_16x16x32_bf16 v[36:39], v[148:151], v[200:203], v[36:39]
	v_mfma_f32_16x16x32_bf16 v[32:35], v[156:159], v[200:203], v[32:35]
	s_setprio 0
	s_barrier
	s_add_u32 s52, s50, 0x8000
	s_addc_u32 s53, s51, 0
	s_mov_b32 m0, s69
	v_lshl_add_u64 v[208:209], s[52:53], 0, v[174:175]
	s_add_u32 s50, s50, 0xc000
	ds_read_b128 v[160:163], v251 offset:49152
	ds_read_b128 v[164:167], v251 offset:50176
	ds_read_b128 v[168:171], v251 offset:51200
	ds_read_b128 v[184:187], v251 offset:52224
	ds_read_b128 v[188:191], v251 offset:53248
	ds_read_b128 v[192:195], v251 offset:54272
	ds_read_b128 v[196:199], v251 offset:55296
	ds_read_b128 v[200:203], v251 offset:56320
	global_load_lds_dwordx4 v[208:209], off
	v_lshl_add_u64 v[208:209], s[52:53], 0, v[178:179]
	s_mov_b32 m0, s70
	s_addc_u32 s51, s51, 0
	global_load_lds_dwordx4 v[208:209], off
	v_lshl_add_u64 v[208:209], s[50:51], 0, v[174:175]
	s_mov_b32 m0, s74
	v_lshl_add_u64 v[204:205], v[204:205], 0, s[26:27]
	global_load_lds_dwordx4 v[208:209], off
	v_lshl_add_u64 v[208:209], s[50:51], 0, v[178:179]
	s_mov_b32 m0, s75
	s_nop 0
	global_load_lds_dwordx4 v[208:209], off
	s_mov_b32 m0, s71
	s_nop 0
	global_load_lds_dwordx4 v[204:205], off
	v_lshl_add_u64 v[204:205], v[206:207], 0, s[26:27]
	s_mov_b32 m0, s72
	s_nop 0
	global_load_lds_dwordx4 v[204:205], off
	s_waitcnt vmcnt(8)
	s_waitcnt lgkmcnt(0)
	s_setprio 1
	s_barrier
	v_mfma_f32_16x16x32_bf16 v[92:95], v[128:131], v[160:163], v[92:95]
	v_mfma_f32_16x16x32_bf16 v[88:91], v[136:139], v[160:163], v[88:91]
	v_mfma_f32_16x16x32_bf16 v[84:87], v[128:131], v[168:171], v[84:87]
	v_mfma_f32_16x16x32_bf16 v[80:83], v[136:139], v[168:171], v[80:83]
	v_mfma_f32_16x16x32_bf16 v[76:79], v[128:131], v[188:191], v[76:79]
	v_mfma_f32_16x16x32_bf16 v[72:75], v[136:139], v[188:191], v[72:75]
	v_mfma_f32_16x16x32_bf16 v[68:71], v[128:131], v[196:199], v[68:71]
	v_mfma_f32_16x16x32_bf16 v[64:67], v[136:139], v[196:199], v[64:67]
	v_mfma_f32_16x16x32_bf16 v[92:95], v[132:135], v[164:167], v[92:95]
	v_mfma_f32_16x16x32_bf16 v[88:91], v[140:143], v[164:167], v[88:91]
	v_mfma_f32_16x16x32_bf16 v[84:87], v[132:135], v[184:187], v[84:87]
	v_mfma_f32_16x16x32_bf16 v[80:83], v[140:143], v[184:187], v[80:83]
	v_mfma_f32_16x16x32_bf16 v[76:79], v[132:135], v[192:195], v[76:79]
	v_mfma_f32_16x16x32_bf16 v[72:75], v[140:143], v[192:195], v[72:75]
	v_mfma_f32_16x16x32_bf16 v[68:71], v[132:135], v[200:203], v[68:71]
	v_mfma_f32_16x16x32_bf16 v[64:67], v[140:143], v[200:203], v[64:67]
	s_setprio 0
	s_setprio 1
	v_mfma_f32_16x16x32_bf16 v[28:31], v[144:147], v[160:163], v[28:31]
	v_mfma_f32_16x16x32_bf16 v[24:27], v[152:155], v[160:163], v[24:27]
	v_mfma_f32_16x16x32_bf16 v[20:23], v[144:147], v[168:171], v[20:23]
	v_mfma_f32_16x16x32_bf16 v[16:19], v[152:155], v[168:171], v[16:19]
	v_mfma_f32_16x16x32_bf16 v[12:15], v[144:147], v[188:191], v[12:15]
	v_mfma_f32_16x16x32_bf16 v[8:11], v[152:155], v[188:191], v[8:11]
	v_mfma_f32_16x16x32_bf16 v[4:7], v[144:147], v[196:199], v[4:7]
	v_mfma_f32_16x16x32_bf16 v[0:3], v[152:155], v[196:199], v[0:3]
	v_mfma_f32_16x16x32_bf16 v[28:31], v[148:151], v[164:167], v[28:31]
	v_mfma_f32_16x16x32_bf16 v[24:27], v[156:159], v[164:167], v[24:27]
	v_mfma_f32_16x16x32_bf16 v[20:23], v[148:151], v[184:187], v[20:23]
	v_mfma_f32_16x16x32_bf16 v[16:19], v[156:159], v[184:187], v[16:19]
	v_mfma_f32_16x16x32_bf16 v[12:15], v[148:151], v[192:195], v[12:15]
	v_mfma_f32_16x16x32_bf16 v[8:11], v[156:159], v[192:195], v[8:11]
	v_mfma_f32_16x16x32_bf16 v[4:7], v[148:151], v[200:203], v[4:7]
	v_mfma_f32_16x16x32_bf16 v[0:3], v[156:159], v[200:203], v[0:3]
	s_setprio 0
	s_barrier
	s_add_i32 s80, s80, 2
	s_add_u32 s49, s49, 0x10000
	s_addc_u32 s55, s55, 0
	s_add_u32 s0, s0, 0x100
	s_addc_u32 s1, s1, 0
	s_cmp_gt_u32 s80, 29
	s_cbranch_scc0 .LBB0_1055
	v_mov_b64_e32 v[220:221], 0x1ff
	v_mov_b64_e32 v[218:219], 0x200
	s_and_b64 vcc, exec, s[34:35]
	s_cbranch_vccz .LBB0_1058
	s_barrier

.LBB0_1172:
	s_ashr_i32 s39, s38, 31
	s_lshl_b64 s[4:5], s[38:39], 20
	s_add_u32 s40, s18, s4
	s_addc_u32 s41, s19, s5
	s_and_b64 s[4:5], s[36:37], exec
	s_cselect_b32 s4, s41, s1
	s_cselect_b32 s5, s40, s0
	s_ashr_i32 s35, s34, 31
	s_lshl_b64 s[42:43], s[34:35], 20
	s_add_u32 s42, s16, s42
	s_addc_u32 s43, s17, s43
	s_and_b64 s[48:49], s[36:37], exec
	s_cselect_b32 s35, s43, s47
	s_cselect_b32 s39, s42, s46
	s_add_u32 s76, s46, 0x10000
	s_addc_u32 s77, s47, 0
	s_mov_b32 s78, -2
	v_add_u32_e32 v124, s28, v156
	v_add_u32_e32 v170, s45, v156
	ds_read_b128 v[108:111], v124
	ds_read_b128 v[112:115], v124 offset:1024
	ds_read_b128 v[120:123], v124 offset:2048
	ds_read_b128 v[124:127], v124 offset:3072
	ds_read_b128 v[158:161], v170
	ds_read_b128 v[162:165], v170 offset:1024
	ds_read_b128 v[166:169], v170 offset:2048
	ds_read_b128 v[170:173], v170 offset:3072
	s_add_u32 s46, s0, 0x10000
	s_addc_u32 s47, s1, 0
	s_cmp_eq_u32 s78, 28
	s_cselect_b32 s52, s5, s46
	s_cselect_b32 s53, s4, s47
	s_cselect_b32 s50, s39, s76
	s_cselect_b32 s51, s35, s77
	s_add_u32 s48, s52, 0x8000
	s_addc_u32 s49, s53, 0
	v_lshl_add_u64 v[206:207], s[0:1], 0, v[152:153]
	s_add_i32 m0, s56, 0xc000
	ds_read_b128 v[174:177], v157
	ds_read_b128 v[178:181], v157 offset:1024
	ds_read_b128 v[182:185], v157 offset:2048
	ds_read_b128 v[186:189], v157 offset:3072
	ds_read_b128 v[190:193], v157 offset:4096
	ds_read_b128 v[194:197], v157 offset:5120
	ds_read_b128 v[198:201], v157 offset:6144
	ds_read_b128 v[202:205], v157 offset:7168
	global_load_lds_dwordx4 v[206:207], off
	v_lshl_add_u64 v[206:207], s[0:1], 0, v[154:155]
	s_add_i32 m0, s56, 0xe000
	s_nop 0
	global_load_lds_dwordx4 v[206:207], off
	s_waitcnt vmcnt(8)
	s_waitcnt lgkmcnt(0)
	s_setprio 1
	s_barrier
	v_mfma_f32_16x16x32_bf16 v[140:143], v[108:111], v[174:177], 0
	v_mfma_f32_16x16x32_bf16 v[136:139], v[120:123], v[174:177], 0
	v_mfma_f32_16x16x32_bf16 v[116:119], v[108:111], v[182:185], 0
	v_mfma_f32_16x16x32_bf16 v[104:107], v[120:123], v[182:185], 0
	v_mfma_f32_16x16x32_bf16 v[92:95], v[108:111], v[190:193], 0
	v_mfma_f32_16x16x32_bf16 v[88:91], v[120:123], v[190:193], 0
	v_mfma_f32_16x16x32_bf16 v[76:79], v[108:111], v[198:201], 0
	v_mfma_f32_16x16x32_bf16 v[72:75], v[120:123], v[198:201], 0
	v_mfma_f32_16x16x32_bf16 v[140:143], v[112:115], v[178:181], v[140:143]
	v_mfma_f32_16x16x32_bf16 v[136:139], v[124:127], v[178:181], v[136:139]
	v_mfma_f32_16x16x32_bf16 v[116:119], v[112:115], v[186:189], v[116:119]
	v_mfma_f32_16x16x32_bf16 v[104:107], v[124:127], v[186:189], v[104:107]
	v_mfma_f32_16x16x32_bf16 v[92:95], v[112:115], v[194:197], v[92:95]
	v_mfma_f32_16x16x32_bf16 v[88:91], v[124:127], v[194:197], v[88:91]
	v_mfma_f32_16x16x32_bf16 v[76:79], v[112:115], v[202:205], v[76:79]
	v_mfma_f32_16x16x32_bf16 v[72:75], v[124:127], v[202:205], v[72:75]
	s_setprio 0
	s_setprio 1
	v_mfma_f32_16x16x32_bf16 v[132:135], v[158:161], v[174:177], 0
	v_mfma_f32_16x16x32_bf16 v[128:131], v[166:169], v[174:177], 0
	v_mfma_f32_16x16x32_bf16 v[100:103], v[158:161], v[182:185], 0
	v_mfma_f32_16x16x32_bf16 v[96:99], v[166:169], v[182:185], 0
	v_mfma_f32_16x16x32_bf16 v[84:87], v[158:161], v[190:193], 0
	v_mfma_f32_16x16x32_bf16 v[80:83], v[166:169], v[190:193], 0
	v_mfma_f32_16x16x32_bf16 v[68:71], v[158:161], v[198:201], 0
	v_mfma_f32_16x16x32_bf16 v[64:67], v[166:169], v[198:201], 0
	v_mfma_f32_16x16x32_bf16 v[132:135], v[162:165], v[178:181], v[132:135]
	v_mfma_f32_16x16x32_bf16 v[128:131], v[170:173], v[178:181], v[128:131]
	v_mfma_f32_16x16x32_bf16 v[100:103], v[162:165], v[186:189], v[100:103]
	v_mfma_f32_16x16x32_bf16 v[96:99], v[170:173], v[186:189], v[96:99]
	v_mfma_f32_16x16x32_bf16 v[84:87], v[162:165], v[194:197], v[84:87]
	v_mfma_f32_16x16x32_bf16 v[80:83], v[170:173], v[194:197], v[80:83]
	v_mfma_f32_16x16x32_bf16 v[68:71], v[162:165], v[202:205], v[68:71]
	v_mfma_f32_16x16x32_bf16 v[64:67], v[170:173], v[202:205], v[64:67]
	s_setprio 0
	s_barrier
	s_mov_b32 m0, s30
	v_lshl_add_u64 v[206:207], s[50:51], 0, v[146:147]
	s_add_u32 s0, s50, 0x4000
	ds_read_b128 v[174:177], v157 offset:16384
	ds_read_b128 v[178:181], v157 offset:17408
	ds_read_b128 v[182:185], v157 offset:18432
	ds_read_b128 v[186:189], v157 offset:19456
	ds_read_b128 v[190:193], v157 offset:20480
	ds_read_b128 v[194:197], v157 offset:21504
	ds_read_b128 v[198:201], v157 offset:22528
	ds_read_b128 v[202:205], v157 offset:23552
	global_load_lds_dwordx4 v[206:207], off
	v_lshl_add_u64 v[206:207], s[50:51], 0, v[150:151]
	s_mov_b32 m0, s31
	s_addc_u32 s1, s51, 0
	global_load_lds_dwordx4 v[206:207], off
	v_lshl_add_u64 v[206:207], s[0:1], 0, v[146:147]
	s_mov_b32 m0, s54
	s_nop 0
	global_load_lds_dwordx4 v[206:207], off
	v_lshl_add_u64 v[206:207], s[0:1], 0, v[150:151]
	s_mov_b32 m0, s55
	s_nop 0
	global_load_lds_dwordx4 v[206:207], off
	v_lshl_add_u64 v[206:207], s[52:53], 0, v[144:145]
	s_mov_b32 m0, s56
	s_nop 0
	global_load_lds_dwordx4 v[206:207], off
	v_lshl_add_u64 v[206:207], s[52:53], 0, v[148:149]
	s_mov_b32 m0, s57
	s_nop 0
	global_load_lds_dwordx4 v[206:207], off
	s_waitcnt vmcnt(8)
	s_waitcnt lgkmcnt(0)
	s_setprio 1
	s_barrier
	v_mfma_f32_16x16x32_bf16 v[60:63], v[108:111], v[174:177], 0
	v_mfma_f32_16x16x32_bf16 v[56:59], v[120:123], v[174:177], 0
	v_mfma_f32_16x16x32_bf16 v[44:47], v[108:111], v[182:185], 0
	v_mfma_f32_16x16x32_bf16 v[40:43], v[120:123], v[182:185], 0
	v_mfma_f32_16x16x32_bf16 v[28:31], v[108:111], v[190:193], 0
	v_mfma_f32_16x16x32_bf16 v[24:27], v[120:123], v[190:193], 0
	v_mfma_f32_16x16x32_bf16 v[12:15], v[108:111], v[198:201], 0
	v_mfma_f32_16x16x32_bf16 v[8:11], v[120:123], v[198:201], 0
	v_mfma_f32_16x16x32_bf16 v[60:63], v[112:115], v[178:181], v[60:63]
	v_mfma_f32_16x16x32_bf16 v[56:59], v[124:127], v[178:181], v[56:59]
	v_mfma_f32_16x16x32_bf16 v[44:47], v[112:115], v[186:189], v[44:47]
	v_mfma_f32_16x16x32_bf16 v[40:43], v[124:127], v[186:189], v[40:43]
	v_mfma_f32_16x16x32_bf16 v[28:31], v[112:115], v[194:197], v[28:31]
	v_mfma_f32_16x16x32_bf16 v[24:27], v[124:127], v[194:197], v[24:27]
	v_mfma_f32_16x16x32_bf16 v[12:15], v[112:115], v[202:205], v[12:15]
	v_mfma_f32_16x16x32_bf16 v[8:11], v[124:127], v[202:205], v[8:11]
	s_setprio 0
	s_setprio 1
	v_mfma_f32_16x16x32_bf16 v[52:55], v[158:161], v[174:177], 0
	v_mfma_f32_16x16x32_bf16 v[48:51], v[166:169], v[174:177], 0
	v_mfma_f32_16x16x32_bf16 v[36:39], v[158:161], v[182:185], 0
	v_mfma_f32_16x16x32_bf16 v[32:35], v[166:169], v[182:185], 0
	v_mfma_f32_16x16x32_bf16 v[20:23], v[158:161], v[190:193], 0
	v_mfma_f32_16x16x32_bf16 v[16:19], v[166:169], v[190:193], 0
	v_mfma_f32_16x16x32_bf16 v[4:7], v[158:161], v[198:201], 0
	v_mfma_f32_16x16x32_bf16 v[0:3], v[166:169], v[198:201], 0
	v_mfma_f32_16x16x32_bf16 v[52:55], v[162:165], v[178:181], v[52:55]
	v_mfma_f32_16x16x32_bf16 v[48:51], v[170:173], v[178:181], v[48:51]
	v_mfma_f32_16x16x32_bf16 v[36:39], v[162:165], v[186:189], v[36:39]
	v_mfma_f32_16x16x32_bf16 v[32:35], v[170:173], v[186:189], v[32:35]
	v_mfma_f32_16x16x32_bf16 v[20:23], v[162:165], v[194:197], v[20:23]
	v_mfma_f32_16x16x32_bf16 v[16:19], v[170:173], v[194:197], v[16:19]
	v_mfma_f32_16x16x32_bf16 v[4:7], v[162:165], v[202:205], v[4:7]
	v_mfma_f32_16x16x32_bf16 v[0:3], v[170:173], v[202:205], v[0:3]
	s_setprio 0
	s_barrier
	v_add_u32_e32 v124, s62, v156
	v_add_u32_e32 v170, s67, v156
	ds_read_b128 v[108:111], v124
	ds_read_b128 v[112:115], v124 offset:1024
	ds_read_b128 v[120:123], v124 offset:2048
	ds_read_b128 v[124:127], v124 offset:3072
	ds_read_b128 v[158:161], v170
	ds_read_b128 v[162:165], v170 offset:1024
	ds_read_b128 v[166:169], v170 offset:2048
	ds_read_b128 v[170:173], v170 offset:3072
	s_add_u32 s0, s52, 0x4000
	s_addc_u32 s1, s53, 0
	s_mov_b32 m0, s58
	v_lshl_add_u64 v[206:207], s[0:1], 0, v[144:145]
	ds_read_b128 v[174:177], v157 offset:32768
	ds_read_b128 v[178:181], v157 offset:33792
	ds_read_b128 v[182:185], v157 offset:34816
	ds_read_b128 v[186:189], v157 offset:35840
	ds_read_b128 v[190:193], v157 offset:36864
	ds_read_b128 v[194:197], v157 offset:37888
	ds_read_b128 v[198:201], v157 offset:38912
	ds_read_b128 v[202:205], v157 offset:39936
	global_load_lds_dwordx4 v[206:207], off
	v_lshl_add_u64 v[206:207], s[0:1], 0, v[148:149]
	s_mov_b32 m0, s59
	s_nop 0
	global_load_lds_dwordx4 v[206:207], off
	s_waitcnt vmcnt(8)
	s_waitcnt lgkmcnt(0)
	s_setprio 1
	s_barrier
	v_mfma_f32_16x16x32_bf16 v[140:143], v[108:111], v[174:177], v[140:143]
	v_mfma_f32_16x16x32_bf16 v[136:139], v[120:123], v[174:177], v[136:139]
	v_mfma_f32_16x16x32_bf16 v[116:119], v[108:111], v[182:185], v[116:119]
	v_mfma_f32_16x16x32_bf16 v[104:107], v[120:123], v[182:185], v[104:107]
	v_mfma_f32_16x16x32_bf16 v[92:95], v[108:111], v[190:193], v[92:95]
	v_mfma_f32_16x16x32_bf16 v[88:91], v[120:123], v[190:193], v[88:91]
	v_mfma_f32_16x16x32_bf16 v[76:79], v[108:111], v[198:201], v[76:79]
	v_mfma_f32_16x16x32_bf16 v[72:75], v[120:123], v[198:201], v[72:75]
	v_mfma_f32_16x16x32_bf16 v[140:143], v[112:115], v[178:181], v[140:143]
	v_mfma_f32_16x16x32_bf16 v[136:139], v[124:127], v[178:181], v[136:139]
	v_mfma_f32_16x16x32_bf16 v[116:119], v[112:115], v[186:189], v[116:119]
	v_mfma_f32_16x16x32_bf16 v[104:107], v[124:127], v[186:189], v[104:107]
	v_mfma_f32_16x16x32_bf16 v[92:95], v[112:115], v[194:197], v[92:95]
	v_mfma_f32_16x16x32_bf16 v[88:91], v[124:127], v[194:197], v[88:91]
	v_mfma_f32_16x16x32_bf16 v[76:79], v[112:115], v[202:205], v[76:79]
	v_mfma_f32_16x16x32_bf16 v[72:75], v[124:127], v[202:205], v[72:75]
	s_setprio 0
	s_setprio 1
	v_mfma_f32_16x16x32_bf16 v[132:135], v[158:161], v[174:177], v[132:135]
	v_mfma_f32_16x16x32_bf16 v[128:131], v[166:169], v[174:177], v[128:131]
	v_mfma_f32_16x16x32_bf16 v[100:103], v[158:161], v[182:185], v[100:103]
	v_mfma_f32_16x16x32_bf16 v[96:99], v[166:169], v[182:185], v[96:99]
	v_mfma_f32_16x16x32_bf16 v[84:87], v[158:161], v[190:193], v[84:87]
	v_mfma_f32_16x16x32_bf16 v[80:83], v[166:169], v[190:193], v[80:83]
	v_mfma_f32_16x16x32_bf16 v[68:71], v[158:161], v[198:201], v[68:71]
	v_mfma_f32_16x16x32_bf16 v[64:67], v[166:169], v[198:201], v[64:67]
	v_mfma_f32_16x16x32_bf16 v[132:135], v[162:165], v[178:181], v[132:135]
	v_mfma_f32_16x16x32_bf16 v[128:131], v[170:173], v[178:181], v[128:131]
	v_mfma_f32_16x16x32_bf16 v[100:103], v[162:165], v[186:189], v[100:103]
	v_mfma_f32_16x16x32_bf16 v[96:99], v[170:173], v[186:189], v[96:99]
	v_mfma_f32_16x16x32_bf16 v[84:87], v[162:165], v[194:197], v[84:87]
	v_mfma_f32_16x16x32_bf16 v[80:83], v[170:173], v[194:197], v[80:83]
	v_mfma_f32_16x16x32_bf16 v[68:71], v[162:165], v[202:205], v[68:71]
	v_mfma_f32_16x16x32_bf16 v[64:67], v[170:173], v[202:205], v[64:67]
	s_setprio 0
	s_barrier
	s_add_u32 s0, s50, 0x8000
	s_addc_u32 s1, s51, 0
	s_mov_b32 m0, s63
	v_lshl_add_u64 v[206:207], s[0:1], 0, v[146:147]
	ds_read_b128 v[174:177], v157 offset:49152
	ds_read_b128 v[178:181], v157 offset:50176
	ds_read_b128 v[182:185], v157 offset:51200
	ds_read_b128 v[186:189], v157 offset:52224
	ds_read_b128 v[190:193], v157 offset:53248
	ds_read_b128 v[194:197], v157 offset:54272
	ds_read_b128 v[198:201], v157 offset:55296
	ds_read_b128 v[202:205], v157 offset:56320
	global_load_lds_dwordx4 v[206:207], off
	v_lshl_add_u64 v[206:207], s[0:1], 0, v[150:151]
	s_add_u32 s0, s50, 0xc000
	s_mov_b32 m0, s64
	s_addc_u32 s1, s51, 0
	global_load_lds_dwordx4 v[206:207], off
	v_lshl_add_u64 v[206:207], s[0:1], 0, v[146:147]
	s_mov_b32 m0, s68
	s_nop 0
	global_load_lds_dwordx4 v[206:207], off
	v_lshl_add_u64 v[206:207], s[0:1], 0, v[150:151]
	s_mov_b32 m0, s69
	s_nop 0
	global_load_lds_dwordx4 v[206:207], off
	v_lshl_add_u64 v[206:207], s[48:49], 0, v[144:145]
	s_mov_b32 m0, s65
	s_nop 0
	global_load_lds_dwordx4 v[206:207], off
	v_lshl_add_u64 v[206:207], s[48:49], 0, v[148:149]
	s_mov_b32 m0, s66
	s_nop 0
	global_load_lds_dwordx4 v[206:207], off
	s_waitcnt vmcnt(8)
	s_waitcnt lgkmcnt(0)
	s_setprio 1
	s_barrier
	v_mfma_f32_16x16x32_bf16 v[60:63], v[108:111], v[174:177], v[60:63]
	v_mfma_f32_16x16x32_bf16 v[56:59], v[120:123], v[174:177], v[56:59]
	v_mfma_f32_16x16x32_bf16 v[44:47], v[108:111], v[182:185], v[44:47]
	v_mfma_f32_16x16x32_bf16 v[40:43], v[120:123], v[182:185], v[40:43]
	v_mfma_f32_16x16x32_bf16 v[28:31], v[108:111], v[190:193], v[28:31]
	v_mfma_f32_16x16x32_bf16 v[24:27], v[120:123], v[190:193], v[24:27]
	v_mfma_f32_16x16x32_bf16 v[12:15], v[108:111], v[198:201], v[12:15]
	v_mfma_f32_16x16x32_bf16 v[8:11], v[120:123], v[198:201], v[8:11]
	v_mfma_f32_16x16x32_bf16 v[60:63], v[112:115], v[178:181], v[60:63]
	v_mfma_f32_16x16x32_bf16 v[56:59], v[124:127], v[178:181], v[56:59]
	v_mfma_f32_16x16x32_bf16 v[44:47], v[112:115], v[186:189], v[44:47]
	v_mfma_f32_16x16x32_bf16 v[40:43], v[124:127], v[186:189], v[40:43]
	v_mfma_f32_16x16x32_bf16 v[28:31], v[112:115], v[194:197], v[28:31]
	v_mfma_f32_16x16x32_bf16 v[24:27], v[124:127], v[194:197], v[24:27]
	v_mfma_f32_16x16x32_bf16 v[12:15], v[112:115], v[202:205], v[12:15]
	v_mfma_f32_16x16x32_bf16 v[8:11], v[124:127], v[202:205], v[8:11]
	s_setprio 0
	s_setprio 1
	v_mfma_f32_16x16x32_bf16 v[52:55], v[158:161], v[174:177], v[52:55]
	v_mfma_f32_16x16x32_bf16 v[48:51], v[166:169], v[174:177], v[48:51]
	v_mfma_f32_16x16x32_bf16 v[36:39], v[158:161], v[182:185], v[36:39]
	v_mfma_f32_16x16x32_bf16 v[32:35], v[166:169], v[182:185], v[32:35]
	v_mfma_f32_16x16x32_bf16 v[20:23], v[158:161], v[190:193], v[20:23]
	v_mfma_f32_16x16x32_bf16 v[16:19], v[166:169], v[190:193], v[16:19]
	v_mfma_f32_16x16x32_bf16 v[4:7], v[158:161], v[198:201], v[4:7]
	v_mfma_f32_16x16x32_bf16 v[0:3], v[166:169], v[198:201], v[0:3]
	v_mfma_f32_16x16x32_bf16 v[52:55], v[162:165], v[178:181], v[52:55]
	v_mfma_f32_16x16x32_bf16 v[48:51], v[170:173], v[178:181], v[48:51]
	v_mfma_f32_16x16x32_bf16 v[36:39], v[162:165], v[186:189], v[36:39]
	v_mfma_f32_16x16x32_bf16 v[32:35], v[170:173], v[186:189], v[32:35]
	v_mfma_f32_16x16x32_bf16 v[20:23], v[162:165], v[194:197], v[20:23]
	v_mfma_f32_16x16x32_bf16 v[16:19], v[170:173], v[194:197], v[16:19]
	v_mfma_f32_16x16x32_bf16 v[4:7], v[162:165], v[202:205], v[4:7]
	v_mfma_f32_16x16x32_bf16 v[0:3], v[170:173], v[202:205], v[0:3]
	s_setprio 0
	s_barrier
	s_add_i32 s78, s78, 2
	s_add_u32 s76, s76, 0x10000
	s_addc_u32 s77, s77, 0
	s_cmp_gt_u32 s78, 29
	s_mov_b64 s[0:1], s[46:47]
.LBB0_1173:
	v_add_u32_e32 v124, s28, v156
	v_add_u32_e32 v170, s45, v156
	ds_read_b128 v[108:111], v124
	ds_read_b128 v[112:115], v124 offset:1024
	ds_read_b128 v[120:123], v124 offset:2048
	ds_read_b128 v[124:127], v124 offset:3072
	ds_read_b128 v[158:161], v170
	ds_read_b128 v[162:165], v170 offset:1024
	ds_read_b128 v[166:169], v170 offset:2048
	ds_read_b128 v[170:173], v170 offset:3072
	s_add_u32 s46, s0, 0x10000
	s_addc_u32 s47, s1, 0
	s_cmp_eq_u32 s78, 28
	s_cselect_b32 s52, s5, s46
	s_cselect_b32 s53, s4, s47
	s_cselect_b32 s50, s39, s76
	s_cselect_b32 s51, s35, s77
	s_add_u32 s48, s52, 0x8000
	s_addc_u32 s49, s53, 0
	v_lshl_add_u64 v[206:207], s[0:1], 0, v[152:153]
	s_add_i32 m0, s56, 0xc000
	ds_read_b128 v[174:177], v157
	ds_read_b128 v[178:181], v157 offset:1024
	ds_read_b128 v[182:185], v157 offset:2048
	ds_read_b128 v[186:189], v157 offset:3072
	ds_read_b128 v[190:193], v157 offset:4096
	ds_read_b128 v[194:197], v157 offset:5120
	ds_read_b128 v[198:201], v157 offset:6144
	ds_read_b128 v[202:205], v157 offset:7168
	global_load_lds_dwordx4 v[206:207], off
	v_lshl_add_u64 v[206:207], s[0:1], 0, v[154:155]
	s_add_i32 m0, s56, 0xe000
	s_nop 0
	global_load_lds_dwordx4 v[206:207], off
	s_waitcnt vmcnt(8)
	s_waitcnt lgkmcnt(0)
	s_setprio 1
	s_barrier
	v_mfma_f32_16x16x32_bf16 v[140:143], v[108:111], v[174:177], v[140:143]
	v_mfma_f32_16x16x32_bf16 v[136:139], v[120:123], v[174:177], v[136:139]
	v_mfma_f32_16x16x32_bf16 v[116:119], v[108:111], v[182:185], v[116:119]
	v_mfma_f32_16x16x32_bf16 v[104:107], v[120:123], v[182:185], v[104:107]
	v_mfma_f32_16x16x32_bf16 v[92:95], v[108:111], v[190:193], v[92:95]
	v_mfma_f32_16x16x32_bf16 v[88:91], v[120:123], v[190:193], v[88:91]
	v_mfma_f32_16x16x32_bf16 v[76:79], v[108:111], v[198:201], v[76:79]
	v_mfma_f32_16x16x32_bf16 v[72:75], v[120:123], v[198:201], v[72:75]
	v_mfma_f32_16x16x32_bf16 v[140:143], v[112:115], v[178:181], v[140:143]
	v_mfma_f32_16x16x32_bf16 v[136:139], v[124:127], v[178:181], v[136:139]
	v_mfma_f32_16x16x32_bf16 v[116:119], v[112:115], v[186:189], v[116:119]
	v_mfma_f32_16x16x32_bf16 v[104:107], v[124:127], v[186:189], v[104:107]
	v_mfma_f32_16x16x32_bf16 v[92:95], v[112:115], v[194:197], v[92:95]
	v_mfma_f32_16x16x32_bf16 v[88:91], v[124:127], v[194:197], v[88:91]
	v_mfma_f32_16x16x32_bf16 v[76:79], v[112:115], v[202:205], v[76:79]
	v_mfma_f32_16x16x32_bf16 v[72:75], v[124:127], v[202:205], v[72:75]
	s_setprio 0
	s_setprio 1
	v_mfma_f32_16x16x32_bf16 v[132:135], v[158:161], v[174:177], v[132:135]
	v_mfma_f32_16x16x32_bf16 v[128:131], v[166:169], v[174:177], v[128:131]
	v_mfma_f32_16x16x32_bf16 v[100:103], v[158:161], v[182:185], v[100:103]
	v_mfma_f32_16x16x32_bf16 v[96:99], v[166:169], v[182:185], v[96:99]
	v_mfma_f32_16x16x32_bf16 v[84:87], v[158:161], v[190:193], v[84:87]
	v_mfma_f32_16x16x32_bf16 v[80:83], v[166:169], v[190:193], v[80:83]
	v_mfma_f32_16x16x32_bf16 v[68:71], v[158:161], v[198:201], v[68:71]
	v_mfma_f32_16x16x32_bf16 v[64:67], v[166:169], v[198:201], v[64:67]
	v_mfma_f32_16x16x32_bf16 v[132:135], v[162:165], v[178:181], v[132:135]
	v_mfma_f32_16x16x32_bf16 v[128:131], v[170:173], v[178:181], v[128:131]
	v_mfma_f32_16x16x32_bf16 v[100:103], v[162:165], v[186:189], v[100:103]
	v_mfma_f32_16x16x32_bf16 v[96:99], v[170:173], v[186:189], v[96:99]
	v_mfma_f32_16x16x32_bf16 v[84:87], v[162:165], v[194:197], v[84:87]
	v_mfma_f32_16x16x32_bf16 v[80:83], v[170:173], v[194:197], v[80:83]
	v_mfma_f32_16x16x32_bf16 v[68:71], v[162:165], v[202:205], v[68:71]
	v_mfma_f32_16x16x32_bf16 v[64:67], v[170:173], v[202:205], v[64:67]
	s_setprio 0
	s_barrier
	s_mov_b32 m0, s30
	v_lshl_add_u64 v[206:207], s[50:51], 0, v[146:147]
	s_add_u32 s0, s50, 0x4000
	ds_read_b128 v[174:177], v157 offset:16384
	ds_read_b128 v[178:181], v157 offset:17408
	ds_read_b128 v[182:185], v157 offset:18432
	ds_read_b128 v[186:189], v157 offset:19456
	ds_read_b128 v[190:193], v157 offset:20480
	ds_read_b128 v[194:197], v157 offset:21504
	ds_read_b128 v[198:201], v157 offset:22528
	ds_read_b128 v[202:205], v157 offset:23552
	global_load_lds_dwordx4 v[206:207], off
	v_lshl_add_u64 v[206:207], s[50:51], 0, v[150:151]
	s_mov_b32 m0, s31
	s_addc_u32 s1, s51, 0
	global_load_lds_dwordx4 v[206:207], off
	v_lshl_add_u64 v[206:207], s[0:1], 0, v[146:147]
	s_mov_b32 m0, s54
	s_nop 0
	global_load_lds_dwordx4 v[206:207], off
	v_lshl_add_u64 v[206:207], s[0:1], 0, v[150:151]
	s_mov_b32 m0, s55
	s_nop 0
	global_load_lds_dwordx4 v[206:207], off
	v_lshl_add_u64 v[206:207], s[52:53], 0, v[144:145]
	s_mov_b32 m0, s56
	s_nop 0
	global_load_lds_dwordx4 v[206:207], off
	v_lshl_add_u64 v[206:207], s[52:53], 0, v[148:149]
	s_mov_b32 m0, s57
	s_nop 0
	global_load_lds_dwordx4 v[206:207], off
	s_waitcnt vmcnt(8)
	s_waitcnt lgkmcnt(0)
	s_setprio 1
	s_barrier
	v_mfma_f32_16x16x32_bf16 v[60:63], v[108:111], v[174:177], v[60:63]
	v_mfma_f32_16x16x32_bf16 v[56:59], v[120:123], v[174:177], v[56:59]
	v_mfma_f32_16x16x32_bf16 v[44:47], v[108:111], v[182:185], v[44:47]
	v_mfma_f32_16x16x32_bf16 v[40:43], v[120:123], v[182:185], v[40:43]
	v_mfma_f32_16x16x32_bf16 v[28:31], v[108:111], v[190:193], v[28:31]
	v_mfma_f32_16x16x32_bf16 v[24:27], v[120:123], v[190:193], v[24:27]
	v_mfma_f32_16x16x32_bf16 v[12:15], v[108:111], v[198:201], v[12:15]
	v_mfma_f32_16x16x32_bf16 v[8:11], v[120:123], v[198:201], v[8:11]
	v_mfma_f32_16x16x32_bf16 v[60:63], v[112:115], v[178:181], v[60:63]
	v_mfma_f32_16x16x32_bf16 v[56:59], v[124:127], v[178:181], v[56:59]
	v_mfma_f32_16x16x32_bf16 v[44:47], v[112:115], v[186:189], v[44:47]
	v_mfma_f32_16x16x32_bf16 v[40:43], v[124:127], v[186:189], v[40:43]
	v_mfma_f32_16x16x32_bf16 v[28:31], v[112:115], v[194:197], v[28:31]
	v_mfma_f32_16x16x32_bf16 v[24:27], v[124:127], v[194:197], v[24:27]
	v_mfma_f32_16x16x32_bf16 v[12:15], v[112:115], v[202:205], v[12:15]
	v_mfma_f32_16x16x32_bf16 v[8:11], v[124:127], v[202:205], v[8:11]
	s_setprio 0
	s_setprio 1
	v_mfma_f32_16x16x32_bf16 v[52:55], v[158:161], v[174:177], v[52:55]
	v_mfma_f32_16x16x32_bf16 v[48:51], v[166:169], v[174:177], v[48:51]
	v_mfma_f32_16x16x32_bf16 v[36:39], v[158:161], v[182:185], v[36:39]
	v_mfma_f32_16x16x32_bf16 v[32:35], v[166:169], v[182:185], v[32:35]
	v_mfma_f32_16x16x32_bf16 v[20:23], v[158:161], v[190:193], v[20:23]
	v_mfma_f32_16x16x32_bf16 v[16:19], v[166:169], v[190:193], v[16:19]
	v_mfma_f32_16x16x32_bf16 v[4:7], v[158:161], v[198:201], v[4:7]
	v_mfma_f32_16x16x32_bf16 v[0:3], v[166:169], v[198:201], v[0:3]
	v_mfma_f32_16x16x32_bf16 v[52:55], v[162:165], v[178:181], v[52:55]
	v_mfma_f32_16x16x32_bf16 v[48:51], v[170:173], v[178:181], v[48:51]
	v_mfma_f32_16x16x32_bf16 v[36:39], v[162:165], v[186:189], v[36:39]
	v_mfma_f32_16x16x32_bf16 v[32:35], v[170:173], v[186:189], v[32:35]
	v_mfma_f32_16x16x32_bf16 v[20:23], v[162:165], v[194:197], v[20:23]
	v_mfma_f32_16x16x32_bf16 v[16:19], v[170:173], v[194:197], v[16:19]
	v_mfma_f32_16x16x32_bf16 v[4:7], v[162:165], v[202:205], v[4:7]
	v_mfma_f32_16x16x32_bf16 v[0:3], v[170:173], v[202:205], v[0:3]
	s_setprio 0
	s_barrier
	v_add_u32_e32 v124, s62, v156
	v_add_u32_e32 v170, s67, v156
	ds_read_b128 v[108:111], v124
	ds_read_b128 v[112:115], v124 offset:1024
	ds_read_b128 v[120:123], v124 offset:2048
	ds_read_b128 v[124:127], v124 offset:3072
	ds_read_b128 v[158:161], v170
	ds_read_b128 v[162:165], v170 offset:1024
	ds_read_b128 v[166:169], v170 offset:2048
	ds_read_b128 v[170:173], v170 offset:3072
	s_add_u32 s0, s52, 0x4000
	s_addc_u32 s1, s53, 0
	s_mov_b32 m0, s58
	v_lshl_add_u64 v[206:207], s[0:1], 0, v[144:145]
	ds_read_b128 v[174:177], v157 offset:32768
	ds_read_b128 v[178:181], v157 offset:33792
	ds_read_b128 v[182:185], v157 offset:34816
	ds_read_b128 v[186:189], v157 offset:35840
	ds_read_b128 v[190:193], v157 offset:36864
	ds_read_b128 v[194:197], v157 offset:37888
	ds_read_b128 v[198:201], v157 offset:38912
	ds_read_b128 v[202:205], v157 offset:39936
	global_load_lds_dwordx4 v[206:207], off
	v_lshl_add_u64 v[206:207], s[0:1], 0, v[148:149]
	s_mov_b32 m0, s59
	s_nop 0
	global_load_lds_dwordx4 v[206:207], off
	s_waitcnt vmcnt(8)
	s_waitcnt lgkmcnt(0)
	s_setprio 1
	s_barrier
	v_mfma_f32_16x16x32_bf16 v[140:143], v[108:111], v[174:177], v[140:143]
	v_mfma_f32_16x16x32_bf16 v[136:139], v[120:123], v[174:177], v[136:139]
	v_mfma_f32_16x16x32_bf16 v[116:119], v[108:111], v[182:185], v[116:119]
	v_mfma_f32_16x16x32_bf16 v[104:107], v[120:123], v[182:185], v[104:107]
	v_mfma_f32_16x16x32_bf16 v[92:95], v[108:111], v[190:193], v[92:95]
	v_mfma_f32_16x16x32_bf16 v[88:91], v[120:123], v[190:193], v[88:91]
	v_mfma_f32_16x16x32_bf16 v[76:79], v[108:111], v[198:201], v[76:79]
	v_mfma_f32_16x16x32_bf16 v[72:75], v[120:123], v[198:201], v[72:75]
	v_mfma_f32_16x16x32_bf16 v[140:143], v[112:115], v[178:181], v[140:143]
	v_mfma_f32_16x16x32_bf16 v[136:139], v[124:127], v[178:181], v[136:139]
	v_mfma_f32_16x16x32_bf16 v[116:119], v[112:115], v[186:189], v[116:119]
	v_mfma_f32_16x16x32_bf16 v[104:107], v[124:127], v[186:189], v[104:107]
	v_mfma_f32_16x16x32_bf16 v[92:95], v[112:115], v[194:197], v[92:95]
	v_mfma_f32_16x16x32_bf16 v[88:91], v[124:127], v[194:197], v[88:91]
	v_mfma_f32_16x16x32_bf16 v[76:79], v[112:115], v[202:205], v[76:79]
	v_mfma_f32_16x16x32_bf16 v[72:75], v[124:127], v[202:205], v[72:75]
	s_setprio 0
	s_setprio 1
	v_mfma_f32_16x16x32_bf16 v[132:135], v[158:161], v[174:177], v[132:135]
	v_mfma_f32_16x16x32_bf16 v[128:131], v[166:169], v[174:177], v[128:131]
	v_mfma_f32_16x16x32_bf16 v[100:103], v[158:161], v[182:185], v[100:103]
	v_mfma_f32_16x16x32_bf16 v[96:99], v[166:169], v[182:185], v[96:99]
	v_mfma_f32_16x16x32_bf16 v[84:87], v[158:161], v[190:193], v[84:87]
	v_mfma_f32_16x16x32_bf16 v[80:83], v[166:169], v[190:193], v[80:83]
	v_mfma_f32_16x16x32_bf16 v[68:71], v[158:161], v[198:201], v[68:71]
	v_mfma_f32_16x16x32_bf16 v[64:67], v[166:169], v[198:201], v[64:67]
	v_mfma_f32_16x16x32_bf16 v[132:135], v[162:165], v[178:181], v[132:135]
	v_mfma_f32_16x16x32_bf16 v[128:131], v[170:173], v[178:181], v[128:131]
	v_mfma_f32_16x16x32_bf16 v[100:103], v[162:165], v[186:189], v[100:103]
	v_mfma_f32_16x16x32_bf16 v[96:99], v[170:173], v[186:189], v[96:99]
	v_mfma_f32_16x16x32_bf16 v[84:87], v[162:165], v[194:197], v[84:87]
	v_mfma_f32_16x16x32_bf16 v[80:83], v[170:173], v[194:197], v[80:83]
	v_mfma_f32_16x16x32_bf16 v[68:71], v[162:165], v[202:205], v[68:71]
	v_mfma_f32_16x16x32_bf16 v[64:67], v[170:173], v[202:205], v[64:67]
	s_setprio 0
	s_barrier
	s_add_u32 s0, s50, 0x8000
	s_addc_u32 s1, s51, 0
	s_mov_b32 m0, s63
	v_lshl_add_u64 v[206:207], s[0:1], 0, v[146:147]
	ds_read_b128 v[174:177], v157 offset:49152
	ds_read_b128 v[178:181], v157 offset:50176
	ds_read_b128 v[182:185], v157 offset:51200
	ds_read_b128 v[186:189], v157 offset:52224
	ds_read_b128 v[190:193], v157 offset:53248
	ds_read_b128 v[194:197], v157 offset:54272
	ds_read_b128 v[198:201], v157 offset:55296
	ds_read_b128 v[202:205], v157 offset:56320
	global_load_lds_dwordx4 v[206:207], off
	v_lshl_add_u64 v[206:207], s[0:1], 0, v[150:151]
	s_add_u32 s0, s50, 0xc000
	s_mov_b32 m0, s64
	s_addc_u32 s1, s51, 0
	global_load_lds_dwordx4 v[206:207], off
	v_lshl_add_u64 v[206:207], s[0:1], 0, v[146:147]
	s_mov_b32 m0, s68
	s_nop 0
	global_load_lds_dwordx4 v[206:207], off
	v_lshl_add_u64 v[206:207], s[0:1], 0, v[150:151]
	s_mov_b32 m0, s69
	s_nop 0
	global_load_lds_dwordx4 v[206:207], off
	v_lshl_add_u64 v[206:207], s[48:49], 0, v[144:145]
	s_mov_b32 m0, s65
	s_nop 0
	global_load_lds_dwordx4 v[206:207], off
	v_lshl_add_u64 v[206:207], s[48:49], 0, v[148:149]
	s_mov_b32 m0, s66
	s_nop 0
	global_load_lds_dwordx4 v[206:207], off
	s_waitcnt vmcnt(8)
	s_waitcnt lgkmcnt(0)
	s_setprio 1
	s_barrier
	v_mfma_f32_16x16x32_bf16 v[60:63], v[108:111], v[174:177], v[60:63]
	v_mfma_f32_16x16x32_bf16 v[56:59], v[120:123], v[174:177], v[56:59]
	v_mfma_f32_16x16x32_bf16 v[44:47], v[108:111], v[182:185], v[44:47]
	v_mfma_f32_16x16x32_bf16 v[40:43], v[120:123], v[182:185], v[40:43]
	v_mfma_f32_16x16x32_bf16 v[28:31], v[108:111], v[190:193], v[28:31]
	v_mfma_f32_16x16x32_bf16 v[24:27], v[120:123], v[190:193], v[24:27]
	v_mfma_f32_16x16x32_bf16 v[12:15], v[108:111], v[198:201], v[12:15]
	v_mfma_f32_16x16x32_bf16 v[8:11], v[120:123], v[198:201], v[8:11]
	v_mfma_f32_16x16x32_bf16 v[60:63], v[112:115], v[178:181], v[60:63]
	v_mfma_f32_16x16x32_bf16 v[56:59], v[124:127], v[178:181], v[56:59]
	v_mfma_f32_16x16x32_bf16 v[44:47], v[112:115], v[186:189], v[44:47]
	v_mfma_f32_16x16x32_bf16 v[40:43], v[124:127], v[186:189], v[40:43]
	v_mfma_f32_16x16x32_bf16 v[28:31], v[112:115], v[194:197], v[28:31]
	v_mfma_f32_16x16x32_bf16 v[24:27], v[124:127], v[194:197], v[24:27]
	v_mfma_f32_16x16x32_bf16 v[12:15], v[112:115], v[202:205], v[12:15]
	v_mfma_f32_16x16x32_bf16 v[8:11], v[124:127], v[202:205], v[8:11]
	s_setprio 0
	s_setprio 1
	v_mfma_f32_16x16x32_bf16 v[52:55], v[158:161], v[174:177], v[52:55]
	v_mfma_f32_16x16x32_bf16 v[48:51], v[166:169], v[174:177], v[48:51]
	v_mfma_f32_16x16x32_bf16 v[36:39], v[158:161], v[182:185], v[36:39]
	v_mfma_f32_16x16x32_bf16 v[32:35], v[166:169], v[182:185], v[32:35]
	v_mfma_f32_16x16x32_bf16 v[20:23], v[158:161], v[190:193], v[20:23]
	v_mfma_f32_16x16x32_bf16 v[16:19], v[166:169], v[190:193], v[16:19]
	v_mfma_f32_16x16x32_bf16 v[4:7], v[158:161], v[198:201], v[4:7]
	v_mfma_f32_16x16x32_bf16 v[0:3], v[166:169], v[198:201], v[0:3]
	v_mfma_f32_16x16x32_bf16 v[52:55], v[162:165], v[178:181], v[52:55]
	v_mfma_f32_16x16x32_bf16 v[48:51], v[170:173], v[178:181], v[48:51]
	v_mfma_f32_16x16x32_bf16 v[36:39], v[162:165], v[186:189], v[36:39]
	v_mfma_f32_16x16x32_bf16 v[32:35], v[170:173], v[186:189], v[32:35]
	v_mfma_f32_16x16x32_bf16 v[20:23], v[162:165], v[194:197], v[20:23]
	v_mfma_f32_16x16x32_bf16 v[16:19], v[170:173], v[194:197], v[16:19]
	v_mfma_f32_16x16x32_bf16 v[4:7], v[162:165], v[202:205], v[4:7]
	v_mfma_f32_16x16x32_bf16 v[0:3], v[170:173], v[202:205], v[0:3]
	s_setprio 0
	s_barrier
	s_add_i32 s78, s78, 2
	s_add_u32 s76, s76, 0x10000
	s_addc_u32 s77, s77, 0
	s_cmp_gt_u32 s78, 29
	s_mov_b64 s[0:1], s[46:47]
	s_cbranch_scc0 .LBB0_1173
	s_and_b64 vcc, exec, s[24:25]
	s_cbranch_vccz .LBB0_1176
	s_barrier

.LBB0_1247:
	s_ashr_i32 s35, s34, 31
	s_lshl_b64 s[4:5], s[34:35], 22
	s_add_u32 s38, s17, s4
	s_addc_u32 s39, s18, s5
	s_and_b64 s[4:5], s[36:37], exec
	s_cselect_b32 s4, s39, s1
	s_cselect_b32 s5, s38, s0
	s_ashr_i32 s25, s24, 31
	s_lshl_b64 s[40:41], s[24:25], 22
	s_add_u32 s40, s19, s40
	s_addc_u32 s41, s28, s41
	s_and_b64 s[46:47], s[36:37], exec
	s_cselect_b32 s25, s41, s45
	s_cselect_b32 s35, s40, s44
	s_add_u32 s74, s44, 0x10000
	s_addc_u32 s75, s45, 0
	s_mov_b32 s76, -2
	v_add_u32_e32 v92, s30, v206
	v_add_u32_e32 v156, s52, v206
	ds_read_b128 v[72:75], v92
	ds_read_b128 v[76:79], v92 offset:1024
	ds_read_b128 v[84:87], v92 offset:2048
	ds_read_b128 v[92:95], v92 offset:3072
	ds_read_b128 v[144:147], v156
	ds_read_b128 v[148:151], v156 offset:1024
	ds_read_b128 v[152:155], v156 offset:2048
	ds_read_b128 v[156:159], v156 offset:3072
	s_add_u32 s44, s0, 0x10000
	s_addc_u32 s45, s1, 0
	s_cmpk_eq_i32 s76, 0x7c
	s_cselect_b32 s50, s5, s44
	s_cselect_b32 s51, s4, s45
	s_cselect_b32 s48, s35, s74
	s_cselect_b32 s49, s25, s75
	s_add_u32 s46, s50, 0x8000
	s_addc_u32 s47, s51, 0
	v_lshl_add_u64 v[204:205], s[0:1], 0, v[180:181]
	s_add_i32 m0, s56, 0xc000
	ds_read_b128 v[160:163], v207
	ds_read_b128 v[164:167], v207 offset:1024
	ds_read_b128 v[168:171], v207 offset:2048
	ds_read_b128 v[184:187], v207 offset:3072
	ds_read_b128 v[188:191], v207 offset:4096
	ds_read_b128 v[192:195], v207 offset:5120
	ds_read_b128 v[196:199], v207 offset:6144
	ds_read_b128 v[200:203], v207 offset:7168
	global_load_lds_dwordx4 v[204:205], off
	v_lshl_add_u64 v[204:205], s[0:1], 0, v[182:183]
	s_add_i32 m0, s56, 0xe000
	s_nop 0
	global_load_lds_dwordx4 v[204:205], off
	s_waitcnt vmcnt(8)
	s_waitcnt lgkmcnt(0)
	s_setprio 1
	s_barrier
	v_mfma_f32_16x16x32_bf16 v[140:143], v[72:75], v[160:163], 0
	v_mfma_f32_16x16x32_bf16 v[136:139], v[84:87], v[160:163], 0
	v_mfma_f32_16x16x32_bf16 v[124:127], v[72:75], v[168:171], 0
	v_mfma_f32_16x16x32_bf16 v[120:123], v[84:87], v[168:171], 0
	v_mfma_f32_16x16x32_bf16 v[108:111], v[72:75], v[188:191], 0
	v_mfma_f32_16x16x32_bf16 v[104:107], v[84:87], v[188:191], 0
	v_mfma_f32_16x16x32_bf16 v[88:91], v[72:75], v[196:199], 0
	v_mfma_f32_16x16x32_bf16 v[80:83], v[84:87], v[196:199], 0
	v_mfma_f32_16x16x32_bf16 v[140:143], v[76:79], v[164:167], v[140:143]
	v_mfma_f32_16x16x32_bf16 v[136:139], v[92:95], v[164:167], v[136:139]
	v_mfma_f32_16x16x32_bf16 v[124:127], v[76:79], v[184:187], v[124:127]
	v_mfma_f32_16x16x32_bf16 v[120:123], v[92:95], v[184:187], v[120:123]
	v_mfma_f32_16x16x32_bf16 v[108:111], v[76:79], v[192:195], v[108:111]
	v_mfma_f32_16x16x32_bf16 v[104:107], v[92:95], v[192:195], v[104:107]
	v_mfma_f32_16x16x32_bf16 v[88:91], v[76:79], v[200:203], v[88:91]
	v_mfma_f32_16x16x32_bf16 v[80:83], v[92:95], v[200:203], v[80:83]
	s_setprio 0
	s_setprio 1
	v_mfma_f32_16x16x32_bf16 v[132:135], v[144:147], v[160:163], 0
	v_mfma_f32_16x16x32_bf16 v[128:131], v[152:155], v[160:163], 0
	v_mfma_f32_16x16x32_bf16 v[116:119], v[144:147], v[168:171], 0
	v_mfma_f32_16x16x32_bf16 v[112:115], v[152:155], v[168:171], 0
	v_mfma_f32_16x16x32_bf16 v[100:103], v[144:147], v[188:191], 0
	v_mfma_f32_16x16x32_bf16 v[96:99], v[152:155], v[188:191], 0
	v_mfma_f32_16x16x32_bf16 v[68:71], v[144:147], v[196:199], 0
	v_mfma_f32_16x16x32_bf16 v[64:67], v[152:155], v[196:199], 0
	v_mfma_f32_16x16x32_bf16 v[132:135], v[148:151], v[164:167], v[132:135]
	v_mfma_f32_16x16x32_bf16 v[128:131], v[156:159], v[164:167], v[128:131]
	v_mfma_f32_16x16x32_bf16 v[116:119], v[148:151], v[184:187], v[116:119]
	v_mfma_f32_16x16x32_bf16 v[112:115], v[156:159], v[184:187], v[112:115]
	v_mfma_f32_16x16x32_bf16 v[100:103], v[148:151], v[192:195], v[100:103]
	v_mfma_f32_16x16x32_bf16 v[96:99], v[156:159], v[192:195], v[96:99]
	v_mfma_f32_16x16x32_bf16 v[68:71], v[148:151], v[200:203], v[68:71]
	v_mfma_f32_16x16x32_bf16 v[64:67], v[156:159], v[200:203], v[64:67]
	s_setprio 0
	s_barrier
	s_mov_b32 m0, s31
	v_lshl_add_u64 v[204:205], s[48:49], 0, v[174:175]
	s_add_u32 s0, s48, 0x4000
	ds_read_b128 v[160:163], v207 offset:16384
	ds_read_b128 v[164:167], v207 offset:17408
	ds_read_b128 v[168:171], v207 offset:18432
	ds_read_b128 v[184:187], v207 offset:19456
	ds_read_b128 v[188:191], v207 offset:20480
	ds_read_b128 v[192:195], v207 offset:21504
	ds_read_b128 v[196:199], v207 offset:22528
	ds_read_b128 v[200:203], v207 offset:23552
	global_load_lds_dwordx4 v[204:205], off
	v_lshl_add_u64 v[204:205], s[48:49], 0, v[178:179]
	s_mov_b32 m0, s43
	s_addc_u32 s1, s49, 0
	global_load_lds_dwordx4 v[204:205], off
	v_lshl_add_u64 v[204:205], s[0:1], 0, v[174:175]
	s_mov_b32 m0, s53
	s_nop 0
	global_load_lds_dwordx4 v[204:205], off
	v_lshl_add_u64 v[204:205], s[0:1], 0, v[178:179]
	s_mov_b32 m0, s54
	s_nop 0
	global_load_lds_dwordx4 v[204:205], off
	v_lshl_add_u64 v[204:205], s[50:51], 0, v[172:173]
	s_mov_b32 m0, s56
	s_nop 0
	global_load_lds_dwordx4 v[204:205], off
	v_lshl_add_u64 v[204:205], s[50:51], 0, v[176:177]
	s_mov_b32 m0, s57
	s_nop 0
	global_load_lds_dwordx4 v[204:205], off
	s_waitcnt vmcnt(8)
	s_waitcnt lgkmcnt(0)
	s_setprio 1
	s_barrier
	v_mfma_f32_16x16x32_bf16 v[60:63], v[72:75], v[160:163], 0
	v_mfma_f32_16x16x32_bf16 v[56:59], v[84:87], v[160:163], 0
	v_mfma_f32_16x16x32_bf16 v[44:47], v[72:75], v[168:171], 0
	v_mfma_f32_16x16x32_bf16 v[40:43], v[84:87], v[168:171], 0
	v_mfma_f32_16x16x32_bf16 v[28:31], v[72:75], v[188:191], 0
	v_mfma_f32_16x16x32_bf16 v[24:27], v[84:87], v[188:191], 0
	v_mfma_f32_16x16x32_bf16 v[12:15], v[72:75], v[196:199], 0
	v_mfma_f32_16x16x32_bf16 v[8:11], v[84:87], v[196:199], 0
	v_mfma_f32_16x16x32_bf16 v[60:63], v[76:79], v[164:167], v[60:63]
	v_mfma_f32_16x16x32_bf16 v[56:59], v[92:95], v[164:167], v[56:59]
	v_mfma_f32_16x16x32_bf16 v[44:47], v[76:79], v[184:187], v[44:47]
	v_mfma_f32_16x16x32_bf16 v[40:43], v[92:95], v[184:187], v[40:43]
	v_mfma_f32_16x16x32_bf16 v[28:31], v[76:79], v[192:195], v[28:31]
	v_mfma_f32_16x16x32_bf16 v[24:27], v[92:95], v[192:195], v[24:27]
	v_mfma_f32_16x16x32_bf16 v[12:15], v[76:79], v[200:203], v[12:15]
	v_mfma_f32_16x16x32_bf16 v[8:11], v[92:95], v[200:203], v[8:11]
	s_setprio 0
	s_setprio 1
	v_mfma_f32_16x16x32_bf16 v[52:55], v[144:147], v[160:163], 0
	v_mfma_f32_16x16x32_bf16 v[48:51], v[152:155], v[160:163], 0
	v_mfma_f32_16x16x32_bf16 v[36:39], v[144:147], v[168:171], 0
	v_mfma_f32_16x16x32_bf16 v[32:35], v[152:155], v[168:171], 0
	v_mfma_f32_16x16x32_bf16 v[20:23], v[144:147], v[188:191], 0
	v_mfma_f32_16x16x32_bf16 v[16:19], v[152:155], v[188:191], 0
	v_mfma_f32_16x16x32_bf16 v[4:7], v[144:147], v[196:199], 0
	v_mfma_f32_16x16x32_bf16 v[0:3], v[152:155], v[196:199], 0
	v_mfma_f32_16x16x32_bf16 v[52:55], v[148:151], v[164:167], v[52:55]
	v_mfma_f32_16x16x32_bf16 v[48:51], v[156:159], v[164:167], v[48:51]
	v_mfma_f32_16x16x32_bf16 v[36:39], v[148:151], v[184:187], v[36:39]
	v_mfma_f32_16x16x32_bf16 v[32:35], v[156:159], v[184:187], v[32:35]
	v_mfma_f32_16x16x32_bf16 v[20:23], v[148:151], v[192:195], v[20:23]
	v_mfma_f32_16x16x32_bf16 v[16:19], v[156:159], v[192:195], v[16:19]
	v_mfma_f32_16x16x32_bf16 v[4:7], v[148:151], v[200:203], v[4:7]
	v_mfma_f32_16x16x32_bf16 v[0:3], v[156:159], v[200:203], v[0:3]
	s_setprio 0
	s_barrier
	v_add_u32_e32 v92, s64, v206
	v_add_u32_e32 v156, s69, v206
	ds_read_b128 v[72:75], v92
	ds_read_b128 v[76:79], v92 offset:1024
	ds_read_b128 v[84:87], v92 offset:2048
	ds_read_b128 v[92:95], v92 offset:3072
	ds_read_b128 v[144:147], v156
	ds_read_b128 v[148:151], v156 offset:1024
	ds_read_b128 v[152:155], v156 offset:2048
	ds_read_b128 v[156:159], v156 offset:3072
	s_add_u32 s0, s50, 0x4000
	s_addc_u32 s1, s51, 0
	s_mov_b32 m0, s58
	v_lshl_add_u64 v[204:205], s[0:1], 0, v[172:173]
	ds_read_b128 v[160:163], v207 offset:32768
	ds_read_b128 v[164:167], v207 offset:33792
	ds_read_b128 v[168:171], v207 offset:34816
	ds_read_b128 v[184:187], v207 offset:35840
	ds_read_b128 v[188:191], v207 offset:36864
	ds_read_b128 v[192:195], v207 offset:37888
	ds_read_b128 v[196:199], v207 offset:38912
	ds_read_b128 v[200:203], v207 offset:39936
	global_load_lds_dwordx4 v[204:205], off
	v_lshl_add_u64 v[204:205], s[0:1], 0, v[176:177]
	s_mov_b32 m0, s59
	s_nop 0
	global_load_lds_dwordx4 v[204:205], off
	s_waitcnt vmcnt(8)
	s_waitcnt lgkmcnt(0)
	s_setprio 1
	s_barrier
	v_mfma_f32_16x16x32_bf16 v[140:143], v[72:75], v[160:163], v[140:143]
	v_mfma_f32_16x16x32_bf16 v[136:139], v[84:87], v[160:163], v[136:139]
	v_mfma_f32_16x16x32_bf16 v[124:127], v[72:75], v[168:171], v[124:127]
	v_mfma_f32_16x16x32_bf16 v[120:123], v[84:87], v[168:171], v[120:123]
	v_mfma_f32_16x16x32_bf16 v[108:111], v[72:75], v[188:191], v[108:111]
	v_mfma_f32_16x16x32_bf16 v[104:107], v[84:87], v[188:191], v[104:107]
	v_mfma_f32_16x16x32_bf16 v[88:91], v[72:75], v[196:199], v[88:91]
	v_mfma_f32_16x16x32_bf16 v[80:83], v[84:87], v[196:199], v[80:83]
	v_mfma_f32_16x16x32_bf16 v[140:143], v[76:79], v[164:167], v[140:143]
	v_mfma_f32_16x16x32_bf16 v[136:139], v[92:95], v[164:167], v[136:139]
	v_mfma_f32_16x16x32_bf16 v[124:127], v[76:79], v[184:187], v[124:127]
	v_mfma_f32_16x16x32_bf16 v[120:123], v[92:95], v[184:187], v[120:123]
	v_mfma_f32_16x16x32_bf16 v[108:111], v[76:79], v[192:195], v[108:111]
	v_mfma_f32_16x16x32_bf16 v[104:107], v[92:95], v[192:195], v[104:107]
	v_mfma_f32_16x16x32_bf16 v[88:91], v[76:79], v[200:203], v[88:91]
	v_mfma_f32_16x16x32_bf16 v[80:83], v[92:95], v[200:203], v[80:83]
	s_setprio 0
	s_setprio 1
	v_mfma_f32_16x16x32_bf16 v[132:135], v[144:147], v[160:163], v[132:135]
	v_mfma_f32_16x16x32_bf16 v[128:131], v[152:155], v[160:163], v[128:131]
	v_mfma_f32_16x16x32_bf16 v[116:119], v[144:147], v[168:171], v[116:119]
	v_mfma_f32_16x16x32_bf16 v[112:115], v[152:155], v[168:171], v[112:115]
	v_mfma_f32_16x16x32_bf16 v[100:103], v[144:147], v[188:191], v[100:103]
	v_mfma_f32_16x16x32_bf16 v[96:99], v[152:155], v[188:191], v[96:99]
	v_mfma_f32_16x16x32_bf16 v[68:71], v[144:147], v[196:199], v[68:71]
	v_mfma_f32_16x16x32_bf16 v[64:67], v[152:155], v[196:199], v[64:67]
	v_mfma_f32_16x16x32_bf16 v[132:135], v[148:151], v[164:167], v[132:135]
	v_mfma_f32_16x16x32_bf16 v[128:131], v[156:159], v[164:167], v[128:131]
	v_mfma_f32_16x16x32_bf16 v[116:119], v[148:151], v[184:187], v[116:119]
	v_mfma_f32_16x16x32_bf16 v[112:115], v[156:159], v[184:187], v[112:115]
	v_mfma_f32_16x16x32_bf16 v[100:103], v[148:151], v[192:195], v[100:103]
	v_mfma_f32_16x16x32_bf16 v[96:99], v[156:159], v[192:195], v[96:99]
	v_mfma_f32_16x16x32_bf16 v[68:71], v[148:151], v[200:203], v[68:71]
	v_mfma_f32_16x16x32_bf16 v[64:67], v[156:159], v[200:203], v[64:67]
	s_setprio 0
	s_barrier
	s_add_u32 s0, s48, 0x8000
	s_addc_u32 s1, s49, 0
	s_mov_b32 m0, s65
	v_lshl_add_u64 v[204:205], s[0:1], 0, v[174:175]
	ds_read_b128 v[160:163], v207 offset:49152
	ds_read_b128 v[164:167], v207 offset:50176
	ds_read_b128 v[168:171], v207 offset:51200
	ds_read_b128 v[184:187], v207 offset:52224
	ds_read_b128 v[188:191], v207 offset:53248
	ds_read_b128 v[192:195], v207 offset:54272
	ds_read_b128 v[196:199], v207 offset:55296
	ds_read_b128 v[200:203], v207 offset:56320
	global_load_lds_dwordx4 v[204:205], off
	v_lshl_add_u64 v[204:205], s[0:1], 0, v[178:179]
	s_add_u32 s0, s48, 0xc000
	s_mov_b32 m0, s66
	s_addc_u32 s1, s49, 0
	global_load_lds_dwordx4 v[204:205], off
	v_lshl_add_u64 v[204:205], s[0:1], 0, v[174:175]
	s_mov_b32 m0, s70
	s_nop 0
	global_load_lds_dwordx4 v[204:205], off
	v_lshl_add_u64 v[204:205], s[0:1], 0, v[178:179]
	s_mov_b32 m0, s71
	s_nop 0
	global_load_lds_dwordx4 v[204:205], off
	v_lshl_add_u64 v[204:205], s[46:47], 0, v[172:173]
	s_mov_b32 m0, s67
	s_nop 0
	global_load_lds_dwordx4 v[204:205], off
	v_lshl_add_u64 v[204:205], s[46:47], 0, v[176:177]
	s_mov_b32 m0, s68
	s_nop 0
	global_load_lds_dwordx4 v[204:205], off
	s_waitcnt vmcnt(8)
	s_waitcnt lgkmcnt(0)
	s_setprio 1
	s_barrier
	v_mfma_f32_16x16x32_bf16 v[60:63], v[72:75], v[160:163], v[60:63]
	v_mfma_f32_16x16x32_bf16 v[56:59], v[84:87], v[160:163], v[56:59]
	v_mfma_f32_16x16x32_bf16 v[44:47], v[72:75], v[168:171], v[44:47]
	v_mfma_f32_16x16x32_bf16 v[40:43], v[84:87], v[168:171], v[40:43]
	v_mfma_f32_16x16x32_bf16 v[28:31], v[72:75], v[188:191], v[28:31]
	v_mfma_f32_16x16x32_bf16 v[24:27], v[84:87], v[188:191], v[24:27]
	v_mfma_f32_16x16x32_bf16 v[12:15], v[72:75], v[196:199], v[12:15]
	v_mfma_f32_16x16x32_bf16 v[8:11], v[84:87], v[196:199], v[8:11]
	v_mfma_f32_16x16x32_bf16 v[60:63], v[76:79], v[164:167], v[60:63]
	v_mfma_f32_16x16x32_bf16 v[56:59], v[92:95], v[164:167], v[56:59]
	v_mfma_f32_16x16x32_bf16 v[44:47], v[76:79], v[184:187], v[44:47]
	v_mfma_f32_16x16x32_bf16 v[40:43], v[92:95], v[184:187], v[40:43]
	v_mfma_f32_16x16x32_bf16 v[28:31], v[76:79], v[192:195], v[28:31]
	v_mfma_f32_16x16x32_bf16 v[24:27], v[92:95], v[192:195], v[24:27]
	v_mfma_f32_16x16x32_bf16 v[12:15], v[76:79], v[200:203], v[12:15]
	v_mfma_f32_16x16x32_bf16 v[8:11], v[92:95], v[200:203], v[8:11]
	s_setprio 0
	s_setprio 1
	v_mfma_f32_16x16x32_bf16 v[52:55], v[144:147], v[160:163], v[52:55]
	v_mfma_f32_16x16x32_bf16 v[48:51], v[152:155], v[160:163], v[48:51]
	v_mfma_f32_16x16x32_bf16 v[36:39], v[144:147], v[168:171], v[36:39]
	v_mfma_f32_16x16x32_bf16 v[32:35], v[152:155], v[168:171], v[32:35]
	v_mfma_f32_16x16x32_bf16 v[20:23], v[144:147], v[188:191], v[20:23]
	v_mfma_f32_16x16x32_bf16 v[16:19], v[152:155], v[188:191], v[16:19]
	v_mfma_f32_16x16x32_bf16 v[4:7], v[144:147], v[196:199], v[4:7]
	v_mfma_f32_16x16x32_bf16 v[0:3], v[152:155], v[196:199], v[0:3]
	v_mfma_f32_16x16x32_bf16 v[52:55], v[148:151], v[164:167], v[52:55]
	v_mfma_f32_16x16x32_bf16 v[48:51], v[156:159], v[164:167], v[48:51]
	v_mfma_f32_16x16x32_bf16 v[36:39], v[148:151], v[184:187], v[36:39]
	v_mfma_f32_16x16x32_bf16 v[32:35], v[156:159], v[184:187], v[32:35]
	v_mfma_f32_16x16x32_bf16 v[20:23], v[148:151], v[192:195], v[20:23]
	v_mfma_f32_16x16x32_bf16 v[16:19], v[156:159], v[192:195], v[16:19]
	v_mfma_f32_16x16x32_bf16 v[4:7], v[148:151], v[200:203], v[4:7]
	v_mfma_f32_16x16x32_bf16 v[0:3], v[156:159], v[200:203], v[0:3]
	s_setprio 0
	s_barrier
	s_add_i32 s76, s76, 2
	s_add_u32 s74, s74, 0x10000
	s_addc_u32 s75, s75, 0
	s_cmpk_gt_u32 s76, 0x7d
	s_mov_b64 s[0:1], s[44:45]
.LBB0_1248:
	v_add_u32_e32 v92, s30, v206
	v_add_u32_e32 v156, s52, v206
	ds_read_b128 v[72:75], v92
	ds_read_b128 v[76:79], v92 offset:1024
	ds_read_b128 v[84:87], v92 offset:2048
	ds_read_b128 v[92:95], v92 offset:3072
	ds_read_b128 v[144:147], v156
	ds_read_b128 v[148:151], v156 offset:1024
	ds_read_b128 v[152:155], v156 offset:2048
	ds_read_b128 v[156:159], v156 offset:3072
	s_add_u32 s44, s0, 0x10000
	s_addc_u32 s45, s1, 0
	s_cmpk_eq_i32 s76, 0x7c
	s_cselect_b32 s50, s5, s44
	s_cselect_b32 s51, s4, s45
	s_cselect_b32 s48, s35, s74
	s_cselect_b32 s49, s25, s75
	s_add_u32 s46, s50, 0x8000
	s_addc_u32 s47, s51, 0
	v_lshl_add_u64 v[204:205], s[0:1], 0, v[180:181]
	s_add_i32 m0, s56, 0xc000
	ds_read_b128 v[160:163], v207
	ds_read_b128 v[164:167], v207 offset:1024
	ds_read_b128 v[168:171], v207 offset:2048
	ds_read_b128 v[184:187], v207 offset:3072
	ds_read_b128 v[188:191], v207 offset:4096
	ds_read_b128 v[192:195], v207 offset:5120
	ds_read_b128 v[196:199], v207 offset:6144
	ds_read_b128 v[200:203], v207 offset:7168
	global_load_lds_dwordx4 v[204:205], off
	v_lshl_add_u64 v[204:205], s[0:1], 0, v[182:183]
	s_add_i32 m0, s56, 0xe000
	s_nop 0
	global_load_lds_dwordx4 v[204:205], off
	s_waitcnt vmcnt(8)
	s_waitcnt lgkmcnt(0)
	s_setprio 1
	s_barrier
	v_mfma_f32_16x16x32_bf16 v[140:143], v[72:75], v[160:163], v[140:143]
	v_mfma_f32_16x16x32_bf16 v[136:139], v[84:87], v[160:163], v[136:139]
	v_mfma_f32_16x16x32_bf16 v[124:127], v[72:75], v[168:171], v[124:127]
	v_mfma_f32_16x16x32_bf16 v[120:123], v[84:87], v[168:171], v[120:123]
	v_mfma_f32_16x16x32_bf16 v[108:111], v[72:75], v[188:191], v[108:111]
	v_mfma_f32_16x16x32_bf16 v[104:107], v[84:87], v[188:191], v[104:107]
	v_mfma_f32_16x16x32_bf16 v[88:91], v[72:75], v[196:199], v[88:91]
	v_mfma_f32_16x16x32_bf16 v[80:83], v[84:87], v[196:199], v[80:83]
	v_mfma_f32_16x16x32_bf16 v[140:143], v[76:79], v[164:167], v[140:143]
	v_mfma_f32_16x16x32_bf16 v[136:139], v[92:95], v[164:167], v[136:139]
	v_mfma_f32_16x16x32_bf16 v[124:127], v[76:79], v[184:187], v[124:127]
	v_mfma_f32_16x16x32_bf16 v[120:123], v[92:95], v[184:187], v[120:123]
	v_mfma_f32_16x16x32_bf16 v[108:111], v[76:79], v[192:195], v[108:111]
	v_mfma_f32_16x16x32_bf16 v[104:107], v[92:95], v[192:195], v[104:107]
	v_mfma_f32_16x16x32_bf16 v[88:91], v[76:79], v[200:203], v[88:91]
	v_mfma_f32_16x16x32_bf16 v[80:83], v[92:95], v[200:203], v[80:83]
	s_setprio 0
	s_setprio 1
	v_mfma_f32_16x16x32_bf16 v[132:135], v[144:147], v[160:163], v[132:135]
	v_mfma_f32_16x16x32_bf16 v[128:131], v[152:155], v[160:163], v[128:131]
	v_mfma_f32_16x16x32_bf16 v[116:119], v[144:147], v[168:171], v[116:119]
	v_mfma_f32_16x16x32_bf16 v[112:115], v[152:155], v[168:171], v[112:115]
	v_mfma_f32_16x16x32_bf16 v[100:103], v[144:147], v[188:191], v[100:103]
	v_mfma_f32_16x16x32_bf16 v[96:99], v[152:155], v[188:191], v[96:99]
	v_mfma_f32_16x16x32_bf16 v[68:71], v[144:147], v[196:199], v[68:71]
	v_mfma_f32_16x16x32_bf16 v[64:67], v[152:155], v[196:199], v[64:67]
	v_mfma_f32_16x16x32_bf16 v[132:135], v[148:151], v[164:167], v[132:135]
	v_mfma_f32_16x16x32_bf16 v[128:131], v[156:159], v[164:167], v[128:131]
	v_mfma_f32_16x16x32_bf16 v[116:119], v[148:151], v[184:187], v[116:119]
	v_mfma_f32_16x16x32_bf16 v[112:115], v[156:159], v[184:187], v[112:115]
	v_mfma_f32_16x16x32_bf16 v[100:103], v[148:151], v[192:195], v[100:103]
	v_mfma_f32_16x16x32_bf16 v[96:99], v[156:159], v[192:195], v[96:99]
	v_mfma_f32_16x16x32_bf16 v[68:71], v[148:151], v[200:203], v[68:71]
	v_mfma_f32_16x16x32_bf16 v[64:67], v[156:159], v[200:203], v[64:67]
	s_setprio 0
	s_barrier
	s_mov_b32 m0, s31
	v_lshl_add_u64 v[204:205], s[48:49], 0, v[174:175]
	s_add_u32 s0, s48, 0x4000
	ds_read_b128 v[160:163], v207 offset:16384
	ds_read_b128 v[164:167], v207 offset:17408
	ds_read_b128 v[168:171], v207 offset:18432
	ds_read_b128 v[184:187], v207 offset:19456
	ds_read_b128 v[188:191], v207 offset:20480
	ds_read_b128 v[192:195], v207 offset:21504
	ds_read_b128 v[196:199], v207 offset:22528
	ds_read_b128 v[200:203], v207 offset:23552
	global_load_lds_dwordx4 v[204:205], off
	v_lshl_add_u64 v[204:205], s[48:49], 0, v[178:179]
	s_mov_b32 m0, s43
	s_addc_u32 s1, s49, 0
	global_load_lds_dwordx4 v[204:205], off
	v_lshl_add_u64 v[204:205], s[0:1], 0, v[174:175]
	s_mov_b32 m0, s53
	s_nop 0
	global_load_lds_dwordx4 v[204:205], off
	v_lshl_add_u64 v[204:205], s[0:1], 0, v[178:179]
	s_mov_b32 m0, s54
	s_nop 0
	global_load_lds_dwordx4 v[204:205], off
	v_lshl_add_u64 v[204:205], s[50:51], 0, v[172:173]
	s_mov_b32 m0, s56
	s_nop 0
	global_load_lds_dwordx4 v[204:205], off
	v_lshl_add_u64 v[204:205], s[50:51], 0, v[176:177]
	s_mov_b32 m0, s57
	s_nop 0
	global_load_lds_dwordx4 v[204:205], off
	s_waitcnt vmcnt(8)
	s_waitcnt lgkmcnt(0)
	s_setprio 1
	s_barrier
	v_mfma_f32_16x16x32_bf16 v[60:63], v[72:75], v[160:163], v[60:63]
	v_mfma_f32_16x16x32_bf16 v[56:59], v[84:87], v[160:163], v[56:59]
	v_mfma_f32_16x16x32_bf16 v[44:47], v[72:75], v[168:171], v[44:47]
	v_mfma_f32_16x16x32_bf16 v[40:43], v[84:87], v[168:171], v[40:43]
	v_mfma_f32_16x16x32_bf16 v[28:31], v[72:75], v[188:191], v[28:31]
	v_mfma_f32_16x16x32_bf16 v[24:27], v[84:87], v[188:191], v[24:27]
	v_mfma_f32_16x16x32_bf16 v[12:15], v[72:75], v[196:199], v[12:15]
	v_mfma_f32_16x16x32_bf16 v[8:11], v[84:87], v[196:199], v[8:11]
	v_mfma_f32_16x16x32_bf16 v[60:63], v[76:79], v[164:167], v[60:63]
	v_mfma_f32_16x16x32_bf16 v[56:59], v[92:95], v[164:167], v[56:59]
	v_mfma_f32_16x16x32_bf16 v[44:47], v[76:79], v[184:187], v[44:47]
	v_mfma_f32_16x16x32_bf16 v[40:43], v[92:95], v[184:187], v[40:43]
	v_mfma_f32_16x16x32_bf16 v[28:31], v[76:79], v[192:195], v[28:31]
	v_mfma_f32_16x16x32_bf16 v[24:27], v[92:95], v[192:195], v[24:27]
	v_mfma_f32_16x16x32_bf16 v[12:15], v[76:79], v[200:203], v[12:15]
	v_mfma_f32_16x16x32_bf16 v[8:11], v[92:95], v[200:203], v[8:11]
	s_setprio 0
	s_setprio 1
	v_mfma_f32_16x16x32_bf16 v[52:55], v[144:147], v[160:163], v[52:55]
	v_mfma_f32_16x16x32_bf16 v[48:51], v[152:155], v[160:163], v[48:51]
	v_mfma_f32_16x16x32_bf16 v[36:39], v[144:147], v[168:171], v[36:39]
	v_mfma_f32_16x16x32_bf16 v[32:35], v[152:155], v[168:171], v[32:35]
	v_mfma_f32_16x16x32_bf16 v[20:23], v[144:147], v[188:191], v[20:23]
	v_mfma_f32_16x16x32_bf16 v[16:19], v[152:155], v[188:191], v[16:19]
	v_mfma_f32_16x16x32_bf16 v[4:7], v[144:147], v[196:199], v[4:7]
	v_mfma_f32_16x16x32_bf16 v[0:3], v[152:155], v[196:199], v[0:3]
	v_mfma_f32_16x16x32_bf16 v[52:55], v[148:151], v[164:167], v[52:55]
	v_mfma_f32_16x16x32_bf16 v[48:51], v[156:159], v[164:167], v[48:51]
	v_mfma_f32_16x16x32_bf16 v[36:39], v[148:151], v[184:187], v[36:39]
	v_mfma_f32_16x16x32_bf16 v[32:35], v[156:159], v[184:187], v[32:35]
	v_mfma_f32_16x16x32_bf16 v[20:23], v[148:151], v[192:195], v[20:23]
	v_mfma_f32_16x16x32_bf16 v[16:19], v[156:159], v[192:195], v[16:19]
	v_mfma_f32_16x16x32_bf16 v[4:7], v[148:151], v[200:203], v[4:7]
	v_mfma_f32_16x16x32_bf16 v[0:3], v[156:159], v[200:203], v[0:3]
	s_setprio 0
	s_barrier
	v_add_u32_e32 v92, s64, v206
	v_add_u32_e32 v156, s69, v206
	ds_read_b128 v[72:75], v92
	ds_read_b128 v[76:79], v92 offset:1024
	ds_read_b128 v[84:87], v92 offset:2048
	ds_read_b128 v[92:95], v92 offset:3072
	ds_read_b128 v[144:147], v156
	ds_read_b128 v[148:151], v156 offset:1024
	ds_read_b128 v[152:155], v156 offset:2048
	ds_read_b128 v[156:159], v156 offset:3072
	s_add_u32 s0, s50, 0x4000
	s_addc_u32 s1, s51, 0
	s_mov_b32 m0, s58
	v_lshl_add_u64 v[204:205], s[0:1], 0, v[172:173]
	ds_read_b128 v[160:163], v207 offset:32768
	ds_read_b128 v[164:167], v207 offset:33792
	ds_read_b128 v[168:171], v207 offset:34816
	ds_read_b128 v[184:187], v207 offset:35840
	ds_read_b128 v[188:191], v207 offset:36864
	ds_read_b128 v[192:195], v207 offset:37888
	ds_read_b128 v[196:199], v207 offset:38912
	ds_read_b128 v[200:203], v207 offset:39936
	global_load_lds_dwordx4 v[204:205], off
	v_lshl_add_u64 v[204:205], s[0:1], 0, v[176:177]
	s_mov_b32 m0, s59
	s_nop 0
	global_load_lds_dwordx4 v[204:205], off
	s_waitcnt vmcnt(8)
	s_waitcnt lgkmcnt(0)
	s_setprio 1
	s_barrier
	v_mfma_f32_16x16x32_bf16 v[140:143], v[72:75], v[160:163], v[140:143]
	v_mfma_f32_16x16x32_bf16 v[136:139], v[84:87], v[160:163], v[136:139]
	v_mfma_f32_16x16x32_bf16 v[124:127], v[72:75], v[168:171], v[124:127]
	v_mfma_f32_16x16x32_bf16 v[120:123], v[84:87], v[168:171], v[120:123]
	v_mfma_f32_16x16x32_bf16 v[108:111], v[72:75], v[188:191], v[108:111]
	v_mfma_f32_16x16x32_bf16 v[104:107], v[84:87], v[188:191], v[104:107]
	v_mfma_f32_16x16x32_bf16 v[88:91], v[72:75], v[196:199], v[88:91]
	v_mfma_f32_16x16x32_bf16 v[80:83], v[84:87], v[196:199], v[80:83]
	v_mfma_f32_16x16x32_bf16 v[140:143], v[76:79], v[164:167], v[140:143]
	v_mfma_f32_16x16x32_bf16 v[136:139], v[92:95], v[164:167], v[136:139]
	v_mfma_f32_16x16x32_bf16 v[124:127], v[76:79], v[184:187], v[124:127]
	v_mfma_f32_16x16x32_bf16 v[120:123], v[92:95], v[184:187], v[120:123]
	v_mfma_f32_16x16x32_bf16 v[108:111], v[76:79], v[192:195], v[108:111]
	v_mfma_f32_16x16x32_bf16 v[104:107], v[92:95], v[192:195], v[104:107]
	v_mfma_f32_16x16x32_bf16 v[88:91], v[76:79], v[200:203], v[88:91]
	v_mfma_f32_16x16x32_bf16 v[80:83], v[92:95], v[200:203], v[80:83]
	s_setprio 0
	s_setprio 1
	v_mfma_f32_16x16x32_bf16 v[132:135], v[144:147], v[160:163], v[132:135]
	v_mfma_f32_16x16x32_bf16 v[128:131], v[152:155], v[160:163], v[128:131]
	v_mfma_f32_16x16x32_bf16 v[116:119], v[144:147], v[168:171], v[116:119]
	v_mfma_f32_16x16x32_bf16 v[112:115], v[152:155], v[168:171], v[112:115]
	v_mfma_f32_16x16x32_bf16 v[100:103], v[144:147], v[188:191], v[100:103]
	v_mfma_f32_16x16x32_bf16 v[96:99], v[152:155], v[188:191], v[96:99]
	v_mfma_f32_16x16x32_bf16 v[68:71], v[144:147], v[196:199], v[68:71]
	v_mfma_f32_16x16x32_bf16 v[64:67], v[152:155], v[196:199], v[64:67]
	v_mfma_f32_16x16x32_bf16 v[132:135], v[148:151], v[164:167], v[132:135]
	v_mfma_f32_16x16x32_bf16 v[128:131], v[156:159], v[164:167], v[128:131]
	v_mfma_f32_16x16x32_bf16 v[116:119], v[148:151], v[184:187], v[116:119]
	v_mfma_f32_16x16x32_bf16 v[112:115], v[156:159], v[184:187], v[112:115]
	v_mfma_f32_16x16x32_bf16 v[100:103], v[148:151], v[192:195], v[100:103]
	v_mfma_f32_16x16x32_bf16 v[96:99], v[156:159], v[192:195], v[96:99]
	v_mfma_f32_16x16x32_bf16 v[68:71], v[148:151], v[200:203], v[68:71]
	v_mfma_f32_16x16x32_bf16 v[64:67], v[156:159], v[200:203], v[64:67]
	s_setprio 0
	s_barrier
	s_add_u32 s0, s48, 0x8000
	s_addc_u32 s1, s49, 0
	s_mov_b32 m0, s65
	v_lshl_add_u64 v[204:205], s[0:1], 0, v[174:175]
	ds_read_b128 v[160:163], v207 offset:49152
	ds_read_b128 v[164:167], v207 offset:50176
	ds_read_b128 v[168:171], v207 offset:51200
	ds_read_b128 v[184:187], v207 offset:52224
	ds_read_b128 v[188:191], v207 offset:53248
	ds_read_b128 v[192:195], v207 offset:54272
	ds_read_b128 v[196:199], v207 offset:55296
	ds_read_b128 v[200:203], v207 offset:56320
	global_load_lds_dwordx4 v[204:205], off
	v_lshl_add_u64 v[204:205], s[0:1], 0, v[178:179]
	s_add_u32 s0, s48, 0xc000
	s_mov_b32 m0, s66
	s_addc_u32 s1, s49, 0
	global_load_lds_dwordx4 v[204:205], off
	v_lshl_add_u64 v[204:205], s[0:1], 0, v[174:175]
	s_mov_b32 m0, s70
	s_nop 0
	global_load_lds_dwordx4 v[204:205], off
	v_lshl_add_u64 v[204:205], s[0:1], 0, v[178:179]
	s_mov_b32 m0, s71
	s_nop 0
	global_load_lds_dwordx4 v[204:205], off
	v_lshl_add_u64 v[204:205], s[46:47], 0, v[172:173]
	s_mov_b32 m0, s67
	s_nop 0
	global_load_lds_dwordx4 v[204:205], off
	v_lshl_add_u64 v[204:205], s[46:47], 0, v[176:177]
	s_mov_b32 m0, s68
	s_nop 0
	global_load_lds_dwordx4 v[204:205], off
	s_waitcnt vmcnt(8)
	s_waitcnt lgkmcnt(0)
	s_setprio 1
	s_barrier
	v_mfma_f32_16x16x32_bf16 v[60:63], v[72:75], v[160:163], v[60:63]
	v_mfma_f32_16x16x32_bf16 v[56:59], v[84:87], v[160:163], v[56:59]
	v_mfma_f32_16x16x32_bf16 v[44:47], v[72:75], v[168:171], v[44:47]
	v_mfma_f32_16x16x32_bf16 v[40:43], v[84:87], v[168:171], v[40:43]
	v_mfma_f32_16x16x32_bf16 v[28:31], v[72:75], v[188:191], v[28:31]
	v_mfma_f32_16x16x32_bf16 v[24:27], v[84:87], v[188:191], v[24:27]
	v_mfma_f32_16x16x32_bf16 v[12:15], v[72:75], v[196:199], v[12:15]
	v_mfma_f32_16x16x32_bf16 v[8:11], v[84:87], v[196:199], v[8:11]
	v_mfma_f32_16x16x32_bf16 v[60:63], v[76:79], v[164:167], v[60:63]
	v_mfma_f32_16x16x32_bf16 v[56:59], v[92:95], v[164:167], v[56:59]
	v_mfma_f32_16x16x32_bf16 v[44:47], v[76:79], v[184:187], v[44:47]
	v_mfma_f32_16x16x32_bf16 v[40:43], v[92:95], v[184:187], v[40:43]
	v_mfma_f32_16x16x32_bf16 v[28:31], v[76:79], v[192:195], v[28:31]
	v_mfma_f32_16x16x32_bf16 v[24:27], v[92:95], v[192:195], v[24:27]
	v_mfma_f32_16x16x32_bf16 v[12:15], v[76:79], v[200:203], v[12:15]
	v_mfma_f32_16x16x32_bf16 v[8:11], v[92:95], v[200:203], v[8:11]
	s_setprio 0
	s_setprio 1
	v_mfma_f32_16x16x32_bf16 v[52:55], v[144:147], v[160:163], v[52:55]
	v_mfma_f32_16x16x32_bf16 v[48:51], v[152:155], v[160:163], v[48:51]
	v_mfma_f32_16x16x32_bf16 v[36:39], v[144:147], v[168:171], v[36:39]
	v_mfma_f32_16x16x32_bf16 v[32:35], v[152:155], v[168:171], v[32:35]
	v_mfma_f32_16x16x32_bf16 v[20:23], v[144:147], v[188:191], v[20:23]
	v_mfma_f32_16x16x32_bf16 v[16:19], v[152:155], v[188:191], v[16:19]
	v_mfma_f32_16x16x32_bf16 v[4:7], v[144:147], v[196:199], v[4:7]
	v_mfma_f32_16x16x32_bf16 v[0:3], v[152:155], v[196:199], v[0:3]
	v_mfma_f32_16x16x32_bf16 v[52:55], v[148:151], v[164:167], v[52:55]
	v_mfma_f32_16x16x32_bf16 v[48:51], v[156:159], v[164:167], v[48:51]
	v_mfma_f32_16x16x32_bf16 v[36:39], v[148:151], v[184:187], v[36:39]
	v_mfma_f32_16x16x32_bf16 v[32:35], v[156:159], v[184:187], v[32:35]
	v_mfma_f32_16x16x32_bf16 v[20:23], v[148:151], v[192:195], v[20:23]
	v_mfma_f32_16x16x32_bf16 v[16:19], v[156:159], v[192:195], v[16:19]
	v_mfma_f32_16x16x32_bf16 v[4:7], v[148:151], v[200:203], v[4:7]
	v_mfma_f32_16x16x32_bf16 v[0:3], v[156:159], v[200:203], v[0:3]
	s_setprio 0
	s_barrier
	s_add_i32 s76, s76, 2
	s_add_u32 s74, s74, 0x10000
	s_addc_u32 s75, s75, 0
	s_cmpk_gt_u32 s76, 0x7d
	s_mov_b64 s[0:1], s[44:45]
	s_cbranch_scc0 .LBB0_1248
	s_and_b64 vcc, exec, s[22:23]
	s_cbranch_vccz .LBB0_1251
	s_barrier
